# rider split 6 tiles in the GQA units / 18 in the differential units (tile counts that keep the GQA ring-slot phase)
# baseline (speedup 1.0000x reference)
; DI f32x16 mfma8(v8i a, v8i b, f32x16 c) { return __builtin_amdgcn_mfma_scale_f32_32x32x64_f8f6f4(a, b, c, 0, 0, 0, 0, 0, 0); }
; DI void attn_unit_d8(unsigned char* lds, const AttnArgs& a) {
;     ...
;     auto tile = [&](const unsigned char* Kb, const unsigned char* Kn, v8i& Pa, v8i& Pb, v8i& v0, v8i& v1, const v8i& Qa, const v8i& Qb, const v8i& w0, const v8i& w1) __attribute__((always_inline)) {
;         qk(Kb, 1, s1a, s1b);
;         v0 = rd32(Kb + voff); v1 = rd32(Kb + voff + 32 * A8_PITCH);
;         o0[0] = mfma8(w0, Qa, o0[0]); o1[0] = mfma8(w0, Qb, o1[0]); o0[1] = mfma8(w1, Qa, o0[1]); o1[1] = mfma8(w1, Qb, o1[1]);
;         expsum(s0a, l0); expsum(s0b, l1); pack4(s0a, Pa, 0); pack4(s0b, Pb, 0);
;         qk(Kn, 0, s0a, s0b);
;         expsum(s1a, l0); expsum(s1b, l1); pack4(s1a, Pa, 4); pack4(s1b, Pb, 4);
; #pragma unroll
;         for (int i = 0; i < 8; ++i) { __builtin_amdgcn_sched_group_barrier(0x008, 1, 0); __builtin_amdgcn_sched_group_barrier(0x402, 22, 0); }
;     };
;     for (int t = a.t0; t < a.t1; t += 2) {
;         const int s1 = sb + 1 >= 5 ? sb - 4 : sb + 1, s2 = sb + 2 >= 5 ? sb - 3 : sb + 2, s3 = sb + 3 >= 5 ? sb - 2 : sb + 3, s4 = sb + 4 >= 5 ? sb - 1 : sb + 4;
;         { const int ta = t + 3, tb = t + 4; gload(ta < a.t1 ? ta : a.t1 - 1, kreg0, vreg0); gload(tb < a.t1 ? tb : a.t1 - 1, kreg1, vreg1); }
;         tile(lds + sb * D8_SLOT, lds + s1 * D8_SLOT, PaX, PbX, vX0, vX1, PaY, PbY, vY0, vY1);
.LBB0_663:
	s_cmp_gt_i32 s16, 3
	s_cselect_b32 s17, -4, 1
	s_add_i32 s18, s17, s16
	s_mul_i32 s6, s16, 0x2800
	s_cmp_gt_i32 s16, 2
	v_mfma_f32_32x32x64_f8f6f4 v[50:65], v[154:161], v[138:145], v[50:65]
	v_exp_f32_e32 v192, v90
	v_add_u32_e32 v90, s6, v218
	s_cselect_b32 s6, -3, 2
	s_add_i32 s6, s6, s16
	s_cmp_gt_i32 s16, 1
	s_cselect_b32 s19, -2, 3
	s_add_i32 s19, s19, s16
	s_cmp_gt_i32 s16, 0
	s_cselect_b32 s49, -1, 4
	s_min_u32 s54, s46, 64
	s_add_i32 s49, s49, s16
	s_cmp_lt_u32 s46, 61
	s_mul_i32 s17, s6, 0x2800
	s_mov_b32 s16, s6
	s_cselect_b64 s[52:53], -1, 0
	s_lshl_b32 s6, s54, 6
	s_add_i32 s54, s6, 0xc0
	s_add_i32 s55, s6, 0xfffff0c0
	s_and_b64 s[52:53], s[52:53], exec
	v_lshl_add_u64 v[98:99], v[182:183], 0, s[6:7]
	s_cselect_b32 s6, s54, s55
	s_cselect_b32 s53, s21, s48
	s_cselect_b32 s52, s20, s47
	s_min_u32 s56, s46, 63
	v_exp_f32_e32 v198, v82
	v_exp_f32_e32 v199, v83
	v_exp_f32_e32 v196, v84
	v_exp_f32_e32 v197, v85
	v_exp_f32_e32 v200, v86
	v_exp_f32_e32 v201, v87
	v_exp_f32_e32 v194, v88
	v_exp_f32_e32 v195, v89
	ds_read_b128 v[82:85], v90 offset:2560
	ds_read_b128 v[86:89], v90 offset:2576
	global_load_dwordx2 v[202:203], v[98:99], off offset:192
	v_add_u32_e32 v98, s6, v215
	s_cmp_lt_u32 s46, 60
	v_ashrrev_i32_e32 v99, 31, v98
	s_cselect_b64 s[54:55], -1, 0
	s_lshl_b32 s6, s56, 6
	v_lshlrev_b64 v[98:99], 8, v[98:99]
	s_add_i32 s56, s6, 0x100
	s_add_i32 s57, s6, 0xfffff100
	v_lshl_add_u64 v[98:99], s[52:53], 0, v[98:99]
	s_and_b64 s[52:53], s[54:55], exec
	s_cselect_b32 s54, s56, s57
	v_lshl_add_u64 v[220:221], v[98:99], 0, v[178:179]
	v_add_u32_e32 v98, s54, v215
	v_ashrrev_i32_e32 v99, 31, v98
	s_cselect_b32 s53, s21, s48
	s_cselect_b32 s52, s20, s47
	v_lshlrev_b64 v[98:99], 8, v[98:99]
	v_lshl_add_u64 v[100:101], v[182:183], 0, s[6:7]
	v_lshl_add_u64 v[98:99], s[52:53], 0, v[98:99]
	global_load_dwordx2 v[204:205], v[100:101], off offset:256
	v_lshl_add_u64 v[222:223], v[98:99], 0, v[178:179]
	s_waitcnt lgkmcnt(0)
	v_mfma_f32_32x32x64_f8f6f4 v[98:113], v[82:89], v[114:121], 0
	v_exp_f32_e32 v193, v91
	v_exp_f32_e32 v224, v92
	v_exp_f32_e32 v225, v93
	v_exp_f32_e32 v226, v94
	v_exp_f32_e32 v227, v95
	v_exp_f32_e32 v228, v96
	v_exp_f32_e32 v229, v97
	ds_read_b128 v[170:173], v90 offset:5120
	ds_read_b128 v[174:177], v90 offset:5136
	ds_read_b128 v[162:165], v90 offset:7680
	ds_read_b128 v[166:169], v90 offset:7696
	v_pk_add_f32 v[90:91], v[186:187], v[198:199]
	v_pk_add_f32 v[92:93], v[184:185], v[196:197]
	v_pk_add_f32 v[90:91], v[200:201], v[90:91]
	v_pk_add_f32 v[92:93], v[194:195], v[92:93]
	v_pk_add_f32 v[90:91], v[192:193], v[90:91]
	v_pk_add_f32 v[92:93], v[224:225], v[92:93]
	v_exp_f32_e32 v66, v66
	v_exp_f32_e32 v67, v67
	v_exp_f32_e32 v68, v68
	v_exp_f32_e32 v69, v69
	v_exp_f32_e32 v70, v70
	v_exp_f32_e32 v71, v71
	v_exp_f32_e32 v72, v72
	v_pk_add_f32 v[230:231], v[228:229], v[92:93]
	v_pk_add_f32 v[232:233], v[226:227], v[90:91]
	v_mfma_f32_32x32x64_f8f6f4 v[82:97], v[82:89], v[122:129], 0
	v_exp_f32_e32 v73, v73
	v_exp_f32_e32 v74, v74
	v_exp_f32_e32 v75, v75
	v_exp_f32_e32 v76, v76
	v_exp_f32_e32 v77, v77
	v_exp_f32_e32 v78, v78
	v_exp_f32_e32 v79, v79
	v_exp_f32_e32 v80, v80
	v_exp_f32_e32 v81, v81
	v_pk_add_f32 v[186:187], v[190:191], v[66:67]
	v_pk_add_f32 v[188:189], v[188:189], v[68:69]
	s_nop 0
	v_pk_add_f32 v[186:187], v[70:71], v[186:187]
	v_pk_add_f32 v[188:189], v[72:73], v[188:189]
	s_nop 0
	v_cvt_scalef32_pk_fp8_f32 v184, v198, v199, s36
	v_pk_add_f32 v[186:187], v[74:75], v[186:187]
	v_pk_add_f32 v[188:189], v[76:77], v[188:189]
	v_cvt_scalef32_pk_fp8_f32 v185, v200, v201, s36
	v_cvt_scalef32_pk_fp8_f32 v184, v196, v197, s36 op_sel:[0,0,0,1]
	v_pk_add_f32 v[190:191], v[78:79], v[186:187]
	v_pk_add_f32 v[188:189], v[80:81], v[188:189]
	v_mfma_f32_32x32x64_f8f6f4 v[2:17], v[154:161], v[130:137], v[2:17]
	s_nop 0
	s_nop 0
	s_nop 0
	s_nop 0
	s_nop 0
	s_nop 0
	s_mulk_i32 s18, 0x2800
	v_cvt_scalef32_pk_fp8_f32 v186, v192, v193, s36
	v_cvt_scalef32_pk_fp8_f32 v187, v226, v227, s36
	v_cvt_scalef32_pk_fp8_f32 v154, v66, v67, s36
	v_cvt_scalef32_pk_fp8_f32 v155, v70, v71, s36
	v_cvt_scalef32_pk_fp8_f32 v156, v74, v75, s36
	v_cvt_scalef32_pk_fp8_f32 v157, v78, v79, s36
	v_cvt_scalef32_pk_fp8_f32 v185, v194, v195, s36 op_sel:[0,0,0,1]
	v_add_u32_e32 v219, s18, v218
	v_cvt_scalef32_pk_fp8_f32 v186, v224, v225, s36 op_sel:[0,0,0,1]
	v_cvt_scalef32_pk_fp8_f32 v187, v228, v229, s36 op_sel:[0,0,0,1]
	v_cvt_scalef32_pk_fp8_f32 v154, v68, v69, s36 op_sel:[0,0,0,1]
	v_cvt_scalef32_pk_fp8_f32 v155, v72, v73, s36 op_sel:[0,0,0,1]
	v_cvt_scalef32_pk_fp8_f32 v156, v76, v77, s36 op_sel:[0,0,0,1]
	v_cvt_scalef32_pk_fp8_f32 v157, v80, v81, s36 op_sel:[0,0,0,1]
	v_exp_f32_e32 v98, v98
	v_exp_f32_e32 v99, v99
	v_mfma_f32_32x32x64_f8f6f4 v[34:49], v[146:153], v[138:145], v[34:49]
	v_exp_f32_e32 v100, v100
	v_exp_f32_e32 v101, v101
	v_exp_f32_e32 v102, v102
	v_exp_f32_e32 v103, v103
	v_exp_f32_e32 v104, v104
	v_exp_f32_e32 v105, v105
	v_exp_f32_e32 v106, v106
	v_exp_f32_e32 v107, v107
	v_exp_f32_e32 v108, v108
	v_exp_f32_e32 v109, v109
	v_exp_f32_e32 v110, v110
	v_exp_f32_e32 v111, v111
	v_exp_f32_e32 v112, v112
	v_exp_f32_e32 v113, v113
	ds_read_b128 v[192:195], v219
	ds_read_b128 v[196:199], v219 offset:16
	v_pk_add_f32 v[66:67], v[232:233], v[98:99]
	v_pk_add_f32 v[68:69], v[230:231], v[100:101]
	v_pk_add_f32 v[66:67], v[102:103], v[66:67]
	v_pk_add_f32 v[68:69], v[104:105], v[68:69]
	v_pk_add_f32 v[66:67], v[106:107], v[66:67]
	v_pk_add_f32 v[68:69], v[108:109], v[68:69]
	v_pk_add_f32 v[140:141], v[110:111], v[66:67]
	v_pk_add_f32 v[138:139], v[112:113], v[68:69]
	v_mfma_f32_32x32x64_f8f6f4 v[18:33], v[146:153], v[130:137], v[18:33]
	v_exp_f32_e32 v82, v82
	v_exp_f32_e32 v83, v83
	v_exp_f32_e32 v84, v84
	v_exp_f32_e32 v85, v85
	v_exp_f32_e32 v86, v86
	v_exp_f32_e32 v87, v87
	v_exp_f32_e32 v88, v88
	v_exp_f32_e32 v89, v89
	v_exp_f32_e32 v90, v90
	v_exp_f32_e32 v91, v91
	v_exp_f32_e32 v92, v92
	v_exp_f32_e32 v93, v93
	v_exp_f32_e32 v94, v94
	v_exp_f32_e32 v95, v95
	v_exp_f32_e32 v96, v96
	v_exp_f32_e32 v97, v97
	v_pk_add_f32 v[66:67], v[190:191], v[82:83]
	v_pk_add_f32 v[68:69], v[188:189], v[84:85]
	v_pk_add_f32 v[66:67], v[86:87], v[66:67]
	v_pk_add_f32 v[68:69], v[88:89], v[68:69]
	v_pk_add_f32 v[130:131], v[90:91], v[66:67]
	v_pk_add_f32 v[132:133], v[92:93], v[68:69]
	s_waitcnt lgkmcnt(0)
; DI KParamsPtr kparams() { KParamsPtr p = (KParamsPtr)__builtin_amdgcn_kernarg_segment_ptr(); asm volatile("" : "+s"(p)); return p; }
; DI void attn_unit_a8(unsigned char* lds, const AttnArgs& a) {
;     ...
;     auto w_decode = [&](int j, const float*& src, unsigned char*& dst, int& ld, int& n0, int& k0, bool& gu) __attribute__((always_inline)) {
;         const int g = (j >> 2) * 512 + a.wl, e = g / 96, rr = g - e * 96; KParamsPtr kp = kparams();
;         if (rr < 64) { src = kp->w_gu + ((size_t)a.wli * NE + e) * (1024 * 2048); dst = kp->ws + WS_WGU + (size_t)a.wli * SZ_WGU + (size_t)e * 2048 * 1024; ld = 2048; n0 = (rr & 7) * 256; k0 = ((rr >> 3) * 4 + (j & 3)) * 32; gu = true; }
;         else { const int q = rr - 64; src = kp->w_dn + ((size_t)a.wli * NE + e) * (1024 * 1024); dst = kp->ws + WS_WDN + (size_t)a.wli * SZ_WDN + (size_t)e * 1024 * 1024; ld = 1024; n0 = (q & 3) * 256; k0 = ((q >> 2) * 4 + (j & 3)) * 32; gu = false; } };
;     auto w_issue = [&](int j) __attribute__((always_inline)) { const float* src; unsigned char* dst; int ld, n0, k0; bool gu; w_decode(j, src, dst, ld, n0, k0, gu);
;         const float* p = src + (size_t)(k0 + 4 * wid) * ld + n0 + wn4;
;         wq[0] = __builtin_nontemporal_load((const f32x4*)p); wq[1] = __builtin_nontemporal_load((const f32x4*)(p + ld));
;         wq[2] = __builtin_nontemporal_load((const f32x4*)(p + (size_t)2 * ld)); wq[3] = __builtin_nontemporal_load((const f32x4*)(p + (size_t)3 * ld)); };
; DI void attn_unit_d8(unsigned char* lds, const AttnArgs& a) {
;     ...
;     auto tile = [&](const unsigned char* Kb, const unsigned char* Kn, v8i& Pa, v8i& Pb, v8i& v0, v8i& v1, const v8i& Qa, const v8i& Qb, const v8i& w0, const v8i& w1) __attribute__((always_inline)) {
;         qk(Kb, 1, s1a, s1b);
;         v0 = rd32(Kb + voff); v1 = rd32(Kb + voff + 32 * A8_PITCH);
;         o0[0] = mfma8(w0, Qa, o0[0]); o1[0] = mfma8(w0, Qb, o1[0]); o0[1] = mfma8(w1, Qa, o0[1]); o1[1] = mfma8(w1, Qb, o1[1]);
;         expsum(s0a, l0); expsum(s0b, l1); pack4(s0a, Pa, 0); pack4(s0b, Pb, 0);
;         qk(Kn, 0, s0a, s0b);
;         expsum(s1a, l0); expsum(s1b, l1); pack4(s1a, Pa, 4); pack4(s1b, Pb, 4);
; #pragma unroll
;         for (int i = 0; i < 8; ++i) { __builtin_amdgcn_sched_group_barrier(0x008, 1, 0); __builtin_amdgcn_sched_group_barrier(0x402, 22, 0); }
;     };
	v_mfma_f32_32x32x64_f8f6f4 v[66:81], v[192:199], v[114:121], 0
	s_nop 0
	s_nop 0
	s_nop 0
	s_nop 0
	s_nop 0
	s_nop 0
	s_nop 0
	v_cvt_scalef32_pk_fp8_f32 v188, v98, v99, s36
	v_cvt_scalef32_pk_fp8_f32 v189, v102, v103, s36
	v_cvt_scalef32_pk_fp8_f32 v190, v106, v107, s36
	v_cvt_scalef32_pk_fp8_f32 v191, v110, v111, s36
	v_cvt_scalef32_pk_fp8_f32 v158, v82, v83, s36
	v_cvt_scalef32_pk_fp8_f32 v159, v86, v87, s36
	v_pk_add_f32 v[142:143], v[96:97], v[132:133]
	v_pk_add_f32 v[144:145], v[94:95], v[130:131]
	v_cvt_scalef32_pk_fp8_f32 v160, v90, v91, s36
	v_cvt_scalef32_pk_fp8_f32 v188, v100, v101, s36 op_sel:[0,0,0,1]
	v_cvt_scalef32_pk_fp8_f32 v189, v104, v105, s36 op_sel:[0,0,0,1]
	v_cvt_scalef32_pk_fp8_f32 v190, v108, v109, s36 op_sel:[0,0,0,1]
	v_cvt_scalef32_pk_fp8_f32 v191, v112, v113, s36 op_sel:[0,0,0,1]
	v_cvt_scalef32_pk_fp8_f32 v158, v84, v85, s36 op_sel:[0,0,0,1]
	v_cvt_scalef32_pk_fp8_f32 v159, v88, v89, s36 op_sel:[0,0,0,1]
	v_mfma_f32_32x32x64_f8f6f4 v[98:113], v[192:199], v[122:129], 0
	global_load_dwordx2 v[192:193], v[220:221], off
	global_load_dwordx2 v[194:195], v[222:223], off
	ds_read_b128 v[130:133], v219 offset:2560
	ds_read_b128 v[134:137], v219 offset:2576
	s_mulk_i32 s19, 0x2800
	s_nop 0
	v_exp_f32_e32 v146, v66
	s_add_i32 s80, s61, 6
	v_exp_f32_e32 v147, v67
	s_lshr_b32 s73, s80, 2
	v_exp_f32_e32 v148, v68
	s_lshl_b32 s73, s73, 9
	v_exp_f32_e32 v149, v69
	s_add_i32 s73, s73, s42
	s_add_i32 s19, s19, 0
	v_cvt_scalef32_pk_fp8_f32 v161, v94, v95, s36
	v_exp_f32_e32 v150, v70
	s_mul_i32 s75, s73, 0xaaab
	v_exp_f32_e32 v151, v71
	s_lshr_b32 s75, s75, 22
	v_exp_f32_e32 v152, v72
	s_mul_i32 s76, s75, 0x60
	v_exp_f32_e32 v153, v73
	s_sub_i32 s76, s73, s76
	v_add_u32_e32 v224, s19, v216
	v_add_u32_e32 v225, s19, v217
	v_cvt_scalef32_pk_fp8_f32 v160, v92, v93, s36 op_sel:[0,0,0,1]
	v_cvt_scalef32_pk_fp8_f32 v161, v96, v97, s36 op_sel:[0,0,0,1]
	v_exp_f32_e32 v196, v74
	s_lshr_b32 s77, s76, 6
	v_exp_f32_e32 v197, v75
	s_lshl_b32 s78, s77, 6
	v_exp_f32_e32 v198, v76
	s_sub_i32 s76, s76, s78
	v_exp_f32_e32 v199, v77
	s_sub_i32 s78, 3, s77
	v_exp_f32_e32 v200, v78
	s_lshr_b32 s79, s76, s78
	v_exp_f32_e32 v201, v79
	s_lshl_b32 s79, s79, 2
	v_exp_f32_e32 v220, v80
	s_and_b32 s81, s80, 3
	v_exp_f32_e32 v221, v81
	s_add_i32 s79, s79, s81
	s_waitcnt lgkmcnt(0)
	v_mfma_f32_32x32x64_f8f6f4 v[82:97], v[130:137], v[114:121], 0
	v_add_f32_e64 v66, v140, v146
	v_add_f32_e64 v67, v141, v147
	v_add_f32_e64 v68, v138, v148
	v_add_f32_e64 v69, v139, v149
	v_add_f32_e64 v66, v150, v66
	v_add_f32_e64 v67, v151, v67
	v_add_f32_e64 v68, v152, v68
	v_add_f32_e64 v69, v153, v69
	v_add_f32_e64 v138, v196, v66
	v_add_f32_e64 v139, v197, v67
	v_add_f32_e64 v140, v198, v68
	v_add_f32_e64 v141, v199, v69
	v_exp_f32_e32 v98, v98
	s_lshl_b32 s79, s79, 5
	v_exp_f32_e32 v99, v99
	s_lshl_b32 s81, s63, 2
	v_exp_f32_e32 v100, v100
	s_add_i32 s81, s81, s79
	v_exp_f32_e32 v101, v101
	s_sub_i32 s78, 13, s77
	v_exp_f32_e32 v102, v102
	s_lshl_b32 s81, s81, s78
	v_exp_f32_e32 v103, v103
	s_lshr_b32 s78, 7, s77
	v_exp_f32_e32 v104, v104
	s_and_b32 s78, s76, s78
	v_exp_f32_e32 v105, v105
	s_lshl_b32 s72, s78, 10
	v_exp_f32_e32 v106, v106
	s_add_i32 s81, s81, s72
	v_exp_f32_e32 v107, v107
	s_add_i32 s72, s75, 0
	v_exp_f32_e32 v108, v108
	s_sub_i32 s80, 23, s77
	v_exp_f32_e32 v109, v109
	s_lshl_b32 s72, s72, s80
	v_exp_f32_e32 v110, v110
	s_add_i32 s81, s81, s72
	v_exp_f32_e32 v111, v111
	s_cmp_eq_u32 s77, 0
	s_cselect_b64 s[84:85], s[66:67], s[68:69]
	v_exp_f32_e32 v112, v112
	s_add_u32 s84, s84, s81
	s_addc_u32 s85, s85, 0
	v_exp_f32_e32 v113, v113
	s_lshr_b32 s80, 0x2000, s77
	v_mfma_f32_32x32x64_f8f6f4 v[66:81], v[130:137], v[122:129], 0
	v_add_f32_e64 v130, v144, v98
	v_add_f32_e64 v131, v145, v99
	v_add_f32_e64 v132, v142, v100
	v_add_f32_e64 v133, v143, v101
	v_add_f32_e64 v142, v102, v130
	v_add_f32_e64 v143, v103, v131
	v_add_f32_e64 v132, v104, v132
	v_add_f32_e64 v133, v105, v133
	v_add_f32_e64 v134, v220, v140
	v_add_f32_e64 v135, v221, v141
	v_add_f32_e64 v136, v200, v138
	v_add_f32_e64 v137, v201, v139
	s_nop 0
	s_nop 0
	s_nop 0
	s_nop 0
	s_nop 0
	s_nop 0
	v_pk_add_f32 v[142:143], v[106:107], v[142:143]
	v_pk_add_f32 v[132:133], v[108:109], v[132:133]
	v_cvt_scalef32_pk_fp8_f32 v138, v146, v147, s36
	v_cvt_scalef32_pk_fp8_f32 v139, v150, v151, s36
	v_cvt_scalef32_pk_fp8_f32 v140, v196, v197, s36
	v_cvt_scalef32_pk_fp8_f32 v141, v200, v201, s36
	v_cvt_scalef32_pk_fp8_f32 v130, v98, v99, s36
	v_cvt_scalef32_pk_fp8_f32 v131, v102, v103, s36
	v_pk_add_f32 v[146:147], v[112:113], v[132:133]
	v_pk_add_f32 v[150:151], v[110:111], v[142:143]
	v_mfma_f32_32x32x64_f8f6f4 v[50:65], v[170:177], v[184:191], v[50:65]
	v_exp_f32_e32 v82, v82
	s_and_b32 s72, s78, 3
	v_exp_f32_e32 v83, v83
	s_lshl_b32 s72, s72, 19
	v_exp_f32_e32 v84, v84
	s_lshr_b32 s81, s78, 2
	v_exp_f32_e32 v85, v85
	s_lshl_b32 s81, s81, 17
	v_add_u32_e32 v102, s17, v218
	v_exp_f32_e32 v86, v86
	s_add_i32 s72, s72, s81
	v_exp_f32_e32 v87, v87
	s_lshl_b32 s81, s78, 18
	v_exp_f32_e32 v88, v88
	s_cmp_eq_u32 s77, 0
	s_cselect_b32 s72, s72, s81
; DI unsigned pk4_fp8_mul64(float a, float b, float c, float d) { v2s_t r = {0, 0}; r = __builtin_amdgcn_cvt_scalef32_pk_fp8_f32(r, a, b, 0.015625f, false); r = __builtin_amdgcn_cvt_scalef32_pk_fp8_f32(r, c, d, 0.015625f, true); return __builtin_bit_cast(unsigned, r); }
; DI f32x16 mfma8(v8i a, v8i b, f32x16 c) { return __builtin_amdgcn_mfma_scale_f32_32x32x64_f8f6f4(a, b, c, 0, 0, 0, 0, 0, 0); }
; DI void attn_unit_a8(unsigned char* lds, const AttnArgs& a) {
;     ...
;     auto w_cvt = [&]() __attribute__((always_inline)) { unsigned char* t8 = lds + AT_WT + wn4 * WPITCH + 4 * wid;
; #pragma unroll
;         for (int j = 0; j < 4; ++j) *(unsigned*)(t8 + j * WPITCH) = pk4_fp8_mul64(wq[0][j], wq[1][j], wq[2][j], wq[3][j]); };
;     const int wcol = tid >> 1, whalf = tid & 1;
;     const unsigned wper_gu = (unsigned)((wcol >> 7) * 256 + (wcol & 96) + invperm32(wcol & 31)) * 1024u + 16u * whalf;
;     const unsigned wper_dn = (unsigned)fwd_lane16(wcol) * 1024u + 16u * whalf;
;     auto w_store = [&](int j) __attribute__((always_inline)) { const float* src; unsigned char* dst; int ld, n0, k0; bool gu; w_decode(j, src, dst, ld, n0, k0, gu);
;         const int nb = n0 >> 8; const unsigned uni = (unsigned)(gu ? (nb & 3) * 512 + (nb >> 2) * 128 : nb * 256) * 1024u + (unsigned)k0;
;         const unsigned off = (gu ? wper_gu : wper_dn) + uni;
;         const unsigned* t = (const unsigned*)(lds + AT_WT + wcol * WPITCH + 16 * whalf);
;         *(u32x4*)(dst + off) = (u32x4){t[0], t[1], t[2], t[3]}; };
; DI void attn_unit_d8(unsigned char* lds, const AttnArgs& a) {
;     ...
;     auto tile = [&](const unsigned char* Kb, const unsigned char* Kn, v8i& Pa, v8i& Pb, v8i& v0, v8i& v1, const v8i& Qa, const v8i& Qb, const v8i& w0, const v8i& w1) __attribute__((always_inline)) {
;         qk(Kb, 1, s1a, s1b);
;         v0 = rd32(Kb + voff); v1 = rd32(Kb + voff + 32 * A8_PITCH);
;         o0[0] = mfma8(w0, Qa, o0[0]); o1[0] = mfma8(w0, Qb, o1[0]); o0[1] = mfma8(w1, Qa, o0[1]); o1[1] = mfma8(w1, Qb, o1[1]);
;         expsum(s0a, l0); expsum(s0b, l1); pack4(s0a, Pa, 0); pack4(s0b, Pb, 0);
;         qk(Kn, 0, s0a, s0b);
;         expsum(s1a, l0); expsum(s1b, l1); pack4(s1a, Pa, 4); pack4(s1b, Pb, 4);
; #pragma unroll
;         for (int i = 0; i < 8; ++i) { __builtin_amdgcn_sched_group_barrier(0x008, 1, 0); __builtin_amdgcn_sched_group_barrier(0x402, 22, 0); }
;     };
	v_exp_f32_e32 v89, v89
	s_mul_i32 s81, s77, 0x10000000
	v_cvt_scalef32_pk_fp8_f32 v130, v100, v101, s36 op_sel:[0,0,0,1]
	v_cvt_scalef32_pk_fp8_f32 v131, v104, v105, s36 op_sel:[0,0,0,1]
	v_exp_f32_e32 v90, v90
	s_add_i32 s81, s81, 0x1094000
	v_exp_f32_e32 v91, v91
	s_add_i32 s72, s72, s79
	v_exp_f32_e32 v92, v92
	s_sub_i32 s73, 21, s77
	v_exp_f32_e32 v93, v93
	s_lshl_b32 s73, s75, s73
	ds_read_b128 v[98:101], v102
	ds_read_b128 v[102:105], v102 offset:16
	s_nop 0
	v_cvt_scalef32_pk_fp8_f32 v138, v148, v149, s36 op_sel:[0,0,0,1]
	v_cvt_scalef32_pk_fp8_f32 v139, v152, v153, s36 op_sel:[0,0,0,1]
	v_cvt_scalef32_pk_fp8_f32 v140, v198, v199, s36 op_sel:[0,0,0,1]
	v_cvt_scalef32_pk_fp8_f32 v141, v220, v221, s36 op_sel:[0,0,0,1]
	s_nop 0
	v_exp_f32_e32 v94, v94
	s_add_i32 s72, s72, s73
	v_mfma_f32_32x32x64_f8f6f4 v[2:17], v[170:177], v[154:161], v[2:17]
	v_exp_f32_e32 v148, v96
	s_add_u32 s72, s72, s81
	v_cvt_scalef32_pk_fp8_f32 v132, v106, v107, s36
	v_exp_f32_e32 v149, v97
	s_or_b32 s79, s72, s77
	v_pk_add_f32 v[96:97], v[136:137], v[82:83]
	v_pk_add_f32 v[106:107], v[134:135], v[84:85]
	v_exp_f32_e32 v66, v66
	v_exp_f32_e32 v67, v67
	v_exp_f32_e32 v68, v68
	v_exp_f32_e32 v69, v69
	v_exp_f32_e32 v95, v95
	v_cvt_scalef32_pk_fp8_f32 v133, v110, v111, s36
	v_pk_add_f32 v[106:107], v[88:89], v[106:107]
	v_pk_add_f32 v[96:97], v[86:87], v[96:97]
	v_exp_f32_e32 v70, v70
	v_exp_f32_e32 v71, v71
	v_exp_f32_e32 v72, v72
	v_exp_f32_e32 v73, v73
	v_cvt_scalef32_pk_fp8_f32 v132, v108, v109, s36 op_sel:[0,0,0,1]
	v_cvt_scalef32_pk_fp8_f32 v133, v112, v113, s36 op_sel:[0,0,0,1]
	v_pk_add_f32 v[96:97], v[90:91], v[96:97]
	v_pk_add_f32 v[106:107], v[92:93], v[106:107]
	v_exp_f32_e32 v74, v74
	v_mfma_f32_32x32x64_f8f6f4 v[34:49], v[162:169], v[184:191], v[34:49]
	v_exp_f32_e32 v75, v75
	v_exp_f32_e32 v76, v76
	v_exp_f32_e32 v77, v77
	v_exp_f32_e32 v78, v78
	v_exp_f32_e32 v79, v79
	s_nop 0
	v_exp_f32_e32 v80, v80
	v_exp_f32_e32 v81, v81
	s_nop 0
	s_nop 0
	v_cvt_scalef32_pk_fp8_f32 v142, v82, v83, s36
	s_nop 0
	v_cvt_scalef32_pk_fp8_f32 v143, v86, v87, s36
	v_cvt_scalef32_pk_fp8_f32 v144, v90, v91, s36
	v_cvt_scalef32_pk_fp8_f32 v142, v84, v85, s36 op_sel:[0,0,0,1]
	v_pk_add_f32 v[82:83], v[150:151], v[66:67]
	v_pk_add_f32 v[84:85], v[146:147], v[68:69]
	s_mulk_i32 s49, 0x2800
	v_pk_add_f32 v[184:185], v[148:149], v[106:107]
	v_pk_add_f32 v[186:187], v[94:95], v[96:97]
	v_cvt_scalef32_pk_fp8_f32 v145, v94, v95, s36
	v_cvt_scalef32_pk_fp8_f32 v143, v88, v89, s36 op_sel:[0,0,0,1]
	v_cvt_scalef32_pk_fp8_f32 v144, v92, v93, s36 op_sel:[0,0,0,1]
	v_mfma_f32_32x32x64_f8f6f4 v[18:33], v[162:169], v[154:161], v[18:33]
	v_add_f32_e64 v84, v72, v84
	v_add_f32_e64 v85, v73, v85
	v_add_f32_e64 v82, v70, v82
	v_add_f32_e64 v83, v71, v83
	s_nop 0
	s_nop 0
	s_nop 0
	s_nop 0
	s_add_i32 s6, s49, 0
	v_add_f32_e64 v82, v74, v82
	v_add_f32_e64 v83, v75, v83
	v_add_f32_e64 v84, v76, v84
	v_add_f32_e64 v85, v77, v85
	v_cvt_scalef32_pk_fp8_f32 v134, v66, v67, s36
	v_cvt_scalef32_pk_fp8_f32 v135, v70, v71, s36
	v_cvt_scalef32_pk_fp8_f32 v136, v74, v75, s36
	v_cvt_scalef32_pk_fp8_f32 v137, v78, v79, s36
	v_pk_add_f32 v[188:189], v[80:81], v[84:85]
	v_pk_add_f32 v[190:191], v[78:79], v[82:83]
	v_add_u32_e32 v106, s6, v216
	v_add_u32_e32 v107, s6, v217
	v_cvt_scalef32_pk_fp8_f32 v145, v148, v149, s36 op_sel:[0,0,0,1]
	v_cvt_scalef32_pk_fp8_f32 v134, v68, v69, s36 op_sel:[0,0,0,1]
	v_cvt_scalef32_pk_fp8_f32 v135, v72, v73, s36 op_sel:[0,0,0,1]
	v_cvt_scalef32_pk_fp8_f32 v136, v76, v77, s36 op_sel:[0,0,0,1]
	v_cvt_scalef32_pk_fp8_f32 v137, v80, v81, s36 op_sel:[0,0,0,1]
	s_waitcnt lgkmcnt(0)
	v_mfma_f32_32x32x64_f8f6f4 v[82:97], v[98:105], v[114:121], 0
	ds_read_b128 v[154:157], v219 offset:5120
	ds_read_b128 v[158:161], v219 offset:5136
	ds_read_b128 v[146:149], v219 offset:7680
	ds_read_b128 v[150:153], v219 offset:7696
	s_cmpk_gt_i32 s42, 0x1ff
	s_cbranch_scc1 .Lmy_rd0_ldum
	s_add_i32 s72, s61, -1
	s_cmp_lt_u32 s72, 18
	s_cbranch_scc0 .Lmy_rd0_noc
	s_waitcnt vmcnt(4)
	v_cvt_scalef32_pk_fp8_f32 v236, v236, v240, s62
	v_cvt_scalef32_pk_fp8_f32 v237, v237, v241, s62
	v_cvt_scalef32_pk_fp8_f32 v238, v238, v242, s62
	v_cvt_scalef32_pk_fp8_f32 v239, v239, v243, s62
	v_cvt_scalef32_pk_fp8_f32 v236, v244, v248, s62 op_sel:[0,0,0,1]
	v_cvt_scalef32_pk_fp8_f32 v237, v245, v249, s62 op_sel:[0,0,0,1]
	v_cvt_scalef32_pk_fp8_f32 v238, v246, v250, s62 op_sel:[0,0,0,1]
	v_cvt_scalef32_pk_fp8_f32 v239, v247, v251, s62 op_sel:[0,0,0,1]
	ds_write_b32 v252, v236
	ds_write_b32 v252, v237 offset:36
	ds_write_b32 v252, v238 offset:72
	ds_write_b32 v252, v239 offset:108
.Lmy_rd0_noc:
	ds_read2_b32 v[244:245], v253 offset1:1
	ds_read2_b32 v[246:247], v253 offset0:2 offset1:3
	s_cmpk_gt_i32 s42, 0x1ff
	s_cbranch_scc1 .Lmy_rd0_sdum
	s_add_i32 s72, s61, -2
	s_cmp_lt_u32 s72, 18
	s_cbranch_scc0 .Lmy_rd0_sdum
	s_andn2_b32 s73, s65, 1
	s_add_u32 s82, s70, s73
	s_addc_u32 s83, s71, 0
	s_bitcmp1_b32 s65, 0
	s_cbranch_scc1 .Lmy_rd0_sdn
	s_waitcnt lgkmcnt(0)
	global_store_dwordx4 v254, v[244:247], s[82:83]
	s_branch .Lmy_rd0_sdone

; DI void attn_unit_a8(unsigned char* lds, const AttnArgs& a) {
;     ...
;         if (hk == 1) { w_cvt(); w_issue(wj + 1 < AT_NWT ? wj + 1 : AT_NWT - 1); }
;         if (hk == 2) w_store(wj);
;         { const int tn = t + 3; gload(tn < a.t1 ? tn : a.t1 - 1, kl, vl); }
.Lmy_rd0_sdone:
	s_cmpk_gt_i32 s42, 0x1ff
	s_cbranch_scc1 .Lmy_rd0_ld0
	s_cmp_lt_u32 s61, 18
	s_cbranch_scc1 .Lmy_rd0_lgo

; DI void attn_unit_a8(unsigned char* lds, const AttnArgs& a) {
;     ...
;     auto w_cvt = [&]() __attribute__((always_inline)) { unsigned char* t8 = lds + AT_WT + wn4 * WPITCH + 4 * wid;
; #pragma unroll
;         for (int j = 0; j < 4; ++j) *(unsigned*)(t8 + j * WPITCH) = pk4_fp8_mul64(wq[0][j], wq[1][j], wq[2][j], wq[3][j]); };
;     const int wcol = tid >> 1, whalf = tid & 1;
;     const unsigned wper_gu = (unsigned)((wcol >> 7) * 256 + (wcol & 96) + invperm32(wcol & 31)) * 1024u + 16u * whalf;
;     const unsigned wper_dn = (unsigned)fwd_lane16(wcol) * 1024u + 16u * whalf;
;     auto w_store = [&](int j) __attribute__((always_inline)) { const float* src; unsigned char* dst; int ld, n0, k0; bool gu; w_decode(j, src, dst, ld, n0, k0, gu);
;         const int nb = n0 >> 8; const unsigned uni = (unsigned)(gu ? (nb & 3) * 512 + (nb >> 2) * 128 : nb * 256) * 1024u + (unsigned)k0;
;         const unsigned off = (gu ? wper_gu : wper_dn) + uni;
;         const unsigned* t = (const unsigned*)(lds + AT_WT + wcol * WPITCH + 16 * whalf);
;         *(u32x4*)(dst + off) = (u32x4){t[0], t[1], t[2], t[3]}; };
;     const bool wrider = a.wl >= 0;
;     if (wrider) w_issue(0);
;     gload(a.t0, kregA, vregA); gload(a.t0 + 1 < a.t1 ? a.t0 + 1 : a.t0, kregB, vregB);
;     lstore(0, kregA, vregA); lstore(1, kregB, vregB);
;     __syncthreads();
;     asm volatile("" : "+v"(qf8));
;     if (a.t0 + 2 < a.t1) gload(a.t0 + 2, kregA, vregA);
;     f32x16 sx0, sx1, sy0, sy1;
;     sx0 = mfma8(kread(lds, 0), qf8, cinit); sx1 = mfma8(kread(lds, 1), qf8, cinit);
;     int slot = 0;
;     auto step = [&](int t, u32x2& kl, u32x2& vl, const u32x2& ks, const u32x2& vs, f32x16& c0, f32x16& c1, f32x16& n0, f32x16& n1, const int hk, const int wj) __attribute__((always_inline)) {
;         const int slot1 = slot == 2 ? 0 : slot + 1, slot2 = slot1 == 2 ? 0 : slot1 + 1;
;         if (hk == 1) { w_cvt(); w_issue(wj + 1 < AT_NWT ? wj + 1 : AT_NWT - 1); }
;         if (hk == 2) w_store(wj);
;         { const int tn = t + 3; gload(tn < a.t1 ? tn : a.t1 - 1, kl, vl); }
;         const unsigned char* Kb = lds + slot * AT_BUFB; const unsigned char* Kn = lds + slot1 * AT_BUFB;
;         const v8i k0 = kread(Kn, 0), k1 = kread(Kn, 1), v0 = vread(Kb, 0), v1 = vread(Kb, 1);
;         n0 = mfma8(k0, qf8, cinit); n1 = mfma8(k1, qf8, cinit);
;         expsum(c0); expsum(c1);
;         const v8i P = pack8(c0, c1);
.LBB0_702:
	s_lshl_b32 s4, s14, 1
	s_waitcnt lgkmcnt(0)
	s_lshr_b32 s12, s14, 3
	s_and_b32 s4, s4, 0x600
	s_and_b32 s12, s12, 0x80
	s_or_b32 s4, s4, s12
	s_and_b64 s[10:11], s[10:11], exec
	s_cselect_b32 s4, s4, s14
	s_and_b32 s10, s24, 3
	s_add_i32 s10, s63, s10
	s_lshl_b32 s10, s10, 5
	s_lshl_b32 s4, s4, 10
	s_add_i32 s15, s4, s10
	s_min_i32 s4, s56, 63
	s_cmp_lt_u32 s56, 60
	s_cselect_b64 s[10:11], -1, 0
	s_lshl_b32 s4, s4, 6
	v_pk_add_f32 v[48:49], v[146:147], v[110:111]
	s_add_i32 s14, s4, 0x100
	s_add_i32 s63, s4, 0xfffff100
	v_pk_add_f32 v[46:47], v[150:151], v[108:109]
	v_pk_add_f32 v[48:49], v[148:149], v[48:49]
	s_and_b64 s[12:13], s[10:11], exec
	v_pk_add_f32 v[46:47], v[142:143], v[46:47]
	v_pk_add_f32 v[48:49], v[58:59], v[48:49]
	s_cselect_b32 s12, s14, s63
	s_add_i32 s25, s25, 1
	v_pk_add_f32 v[46:47], v[144:145], v[46:47]
	v_pk_add_f32 v[48:49], v[60:61], v[48:49]
	s_and_b64 s[6:7], s[6:7], exec
	v_pk_add_f32 v[46:47], v[52:53], v[46:47]
	v_pk_add_f32 v[48:49], v[50:51], v[48:49]
	s_cselect_b32 s14, 0, s25
	v_pk_add_f32 v[46:47], v[56:57], v[46:47]
	v_pk_add_f32 v[48:49], v[54:55], v[48:49]
	s_mul_i32 s6, s14, 0x4680
	v_pk_add_f32 v[38:39], v[38:39], v[46:47]
	v_pk_add_f32 v[36:37], v[36:37], v[48:49]
	v_add_u32_e32 v48, 0xd808, v163
	v_add_u32_e32 v134, s6, v157
	v_pk_add_f32 v[50:51], v[42:43], v[38:39]
	v_pk_add_f32 v[108:109], v[40:41], v[36:37]
	v_add_u32_e32 v45, 0xd800, v163
	ds_read_b128 v[36:39], v134
	ds_read_b128 v[40:43], v134 offset:16
	ds_read2_b32 v[46:47], v45 offset1:1
	ds_read2_b32 v[48:49], v48 offset1:1
	v_pk_add_f32 v[110:111], v[34:35], v[50:51]
	v_add_u32_e32 v34, v44, v158
	v_lshl_or_b32 v34, v34, 10, v160
	v_add_u32_e32 v34, s15, v34
	s_waitcnt lgkmcnt(0)
	global_store_dwordx4 v34, v[46:49], s[8:9]
	v_add_u32_e32 v34, s12, v154
	s_and_b64 s[8:9], s[10:11], exec
	v_ashrrev_i32_e32 v35, 31, v34
	s_cselect_b32 s9, s59, s61
	s_cselect_b32 s8, s58, s60
	v_lshlrev_b64 v[34:35], 7, v[34:35]
	v_mfma_f32_32x32x64_f8f6f4 v[50:65], v[36:43], v[98:105], 0
	v_lshl_add_u64 v[42:43], s[8:9], 0, v[34:35]
	v_lshl_add_u64 v[42:43], v[42:43], 0, v[130:131]
	ds_read_b128 v[34:37], v134 offset:2560
	ds_read_b128 v[38:41], v134 offset:2576
	global_load_dwordx2 v[134:135], v[42:43], off
	v_lshl_add_u64 v[42:43], v[132:133], 0, s[4:5]
	global_load_dwordx2 v[136:137], v[42:43], off offset:256
	v_exp_f32_e32 v82, v82
	v_exp_f32_e32 v83, v83
	v_exp_f32_e32 v86, v86
	v_exp_f32_e32 v87, v87
	v_exp_f32_e32 v90, v90
	v_exp_f32_e32 v91, v91
	v_exp_f32_e32 v94, v94
	v_exp_f32_e32 v95, v95
	v_exp_f32_e32 v150, v66
	v_exp_f32_e32 v151, v67
	v_exp_f32_e32 v174, v70
	v_exp_f32_e32 v175, v71
	v_exp_f32_e32 v74, v74
	v_exp_f32_e32 v75, v75
	v_exp_f32_e32 v78, v78
	v_exp_f32_e32 v79, v79
	ds_read_b128 v[142:145], v164 offset:5120
	ds_read_b128 v[146:149], v164 offset:5136
	ds_read_b128 v[166:169], v164 offset:7680
	ds_read_b128 v[170:173], v164 offset:7696
	v_exp_f32_e32 v84, v84
	v_exp_f32_e32 v85, v85
	v_exp_f32_e32 v88, v88
	v_exp_f32_e32 v89, v89
	v_exp_f32_e32 v92, v92
	v_exp_f32_e32 v93, v93
	v_exp_f32_e32 v96, v96
	v_exp_f32_e32 v97, v97
	v_exp_f32_e32 v164, v68
	v_exp_f32_e32 v165, v69
	v_exp_f32_e32 v176, v72
	v_exp_f32_e32 v177, v73
	v_exp_f32_e32 v76, v76
	v_exp_f32_e32 v77, v77
	v_exp_f32_e32 v80, v80
	v_exp_f32_e32 v81, v81
	s_nop 0
	s_nop 0
	s_nop 0
	s_nop 0
	s_nop 0
	s_nop 0
	s_nop 0
	s_nop 0
	v_cvt_scalef32_pk_fp8_f32 v66, v82, v83, s48
	v_cvt_scalef32_pk_fp8_f32 v70, v150, v151, s48
	v_cvt_scalef32_pk_fp8_f32 v67, v86, v87, s48
	v_cvt_scalef32_pk_fp8_f32 v71, v174, v175, s48
	v_cvt_scalef32_pk_fp8_f32 v68, v90, v91, s48
	v_cvt_scalef32_pk_fp8_f32 v72, v74, v75, s48
	v_cvt_scalef32_pk_fp8_f32 v69, v94, v95, s48
	v_cvt_scalef32_pk_fp8_f32 v73, v78, v79, s48
	v_cvt_scalef32_pk_fp8_f32 v66, v84, v85, s48 op_sel:[0,0,0,1]
	v_cvt_scalef32_pk_fp8_f32 v70, v164, v165, s48 op_sel:[0,0,0,1]
	v_cvt_scalef32_pk_fp8_f32 v67, v88, v89, s48 op_sel:[0,0,0,1]
	v_cvt_scalef32_pk_fp8_f32 v71, v176, v177, s48 op_sel:[0,0,0,1]
	v_cvt_scalef32_pk_fp8_f32 v68, v92, v93, s48 op_sel:[0,0,0,1]
	v_cvt_scalef32_pk_fp8_f32 v72, v76, v77, s48 op_sel:[0,0,0,1]
	v_cvt_scalef32_pk_fp8_f32 v69, v96, v97, s48 op_sel:[0,0,0,1]
	v_cvt_scalef32_pk_fp8_f32 v73, v80, v81, s48 op_sel:[0,0,0,1]
	s_waitcnt lgkmcnt(4)
	v_mfma_f32_32x32x64_f8f6f4 v[34:49], v[34:41], v[98:105], 0
	v_add_f32_e64 v110, v110, v82
	v_add_f32_e64 v111, v111, v83
	v_add_f32_e64 v82, v108, v84
	v_add_f32_e64 v83, v109, v85
	v_add_f32_e64 v84, v86, v110
	v_add_f32_e64 v85, v87, v111
	v_add_f32_e64 v82, v88, v82
	v_add_f32_e64 v83, v89, v83
	s_addk_i32 s6, 0x4680
	v_add_f32_e64 v84, v90, v84
	v_add_f32_e64 v85, v91, v85
	v_add_f32_e64 v82, v92, v82
	v_add_f32_e64 v83, v93, v83
	s_cmp_lg_u32 s14, 2
	v_pk_add_f32 v[82:83], v[96:97], v[82:83]
	v_pk_add_f32 v[84:85], v[94:95], v[84:85]
	s_cselect_b32 s4, s6, 0
	v_pk_add_f32 v[84:85], v[150:151], v[84:85]
	v_pk_add_f32 v[82:83], v[164:165], v[82:83]
	s_add_i32 s4, s4, 0
	v_pk_add_f32 v[82:83], v[176:177], v[82:83]
	s_waitcnt lgkmcnt(2)
	v_mfma_f32_32x32x64_f8f6f4 v[18:33], v[142:149], v[66:73], v[18:33]
	v_add_f32_e64 v84, v174, v84
	v_add_f32_e64 v85, v175, v85
	v_add_f32_e64 v76, v76, v82
	v_add_f32_e64 v77, v77, v83
	v_add_f32_e64 v74, v74, v84
	v_add_f32_e64 v75, v75, v85
	s_add_i32 s24, s24, 1
	s_add_i32 s56, s56, 2
	s_addk_i32 s19, 0x80
	v_add_f32_e64 v110, v80, v76
	v_add_f32_e64 v111, v81, v77
	v_add_f32_e64 v108, v78, v74
	v_add_f32_e64 v109, v79, v75
	s_cmp_lg_u32 s24, 6
	s_waitcnt lgkmcnt(0)
	v_mfma_f32_32x32x64_f8f6f4 v[2:17], v[166:173], v[66:73], v[2:17]
	v_add_u32_e32 v66, s4, v155
	s_waitcnt vmcnt(4)
	ds_write_b64 v66, v[138:139]
	v_add_u32_e32 v66, s4, v156
	v_add_u32_e32 v66, 0x1400, v66
	s_waitcnt vmcnt(3)
	ds_write2_b32 v66, v140, v141 offset1:8
	s_waitcnt lgkmcnt(0)
	s_barrier
	s_cbranch_scc0 .LBB0_712
.LBB0_703:
	s_min_u32 s15, s24, 4
	s_add_i32 s15, s15, 1
	s_lshl_b32 s4, s15, 7
	s_and_b32 s4, s4, 0x1e00
	s_nop 0
	s_nop 0
	s_add_i32 s6, s4, s62
	v_cvt_scalef32_pk_fp8_f32 v66, v116, v112, s47
	v_cvt_scalef32_pk_fp8_f32 v67, v117, v113, s47
	s_mul_hi_u32 s4, s6, 0xaaaaaaab
	v_cvt_scalef32_pk_fp8_f32 v66, v120, v124, s47 op_sel:[0,0,0,1]
	v_cvt_scalef32_pk_fp8_f32 v67, v121, v125, s47 op_sel:[0,0,0,1]
	v_add_u32_e32 v68, 0xd800, v162
	s_lshr_b32 s4, s4, 6
	ds_write2_b32 v68, v66, v67 offset1:9
	s_nop 0
	s_nop 0
	s_mul_i32 s63, s4, 0xffffffa0
	v_cvt_scalef32_pk_fp8_f32 v66, v118, v114, s47
	v_cvt_scalef32_pk_fp8_f32 v67, v119, v115, s47
	s_add_i32 s63, s63, s6
	v_cvt_scalef32_pk_fp8_f32 v66, v122, v126, s47 op_sel:[0,0,0,1]
	v_cvt_scalef32_pk_fp8_f32 v67, v123, v127, s47 op_sel:[0,0,0,1]
	s_mov_b64 s[10:11], s[0:1]
	s_cmp_gt_i32 s63, 63
	s_mov_b64 s[12:13], -1
	ds_write2_b32 v68, v66, v67 offset0:18 offset1:27
	s_cbranch_scc0 .LBB0_705
	s_load_dwordx2 s[6:7], s[10:11], 0xc0
	s_lshl_b64 s[8:9], s[4:5], 22
	s_mov_b64 s[12:13], 0
	s_waitcnt lgkmcnt(0)
	s_add_u32 s6, s6, s8
	s_addc_u32 s7, s7, s9
	s_and_b32 s8, s63, 0x7ffffffc
	s_sub_i32 s25, s8, 64

; DI f32x16 mfma8(v8i a, v8i b, f32x16 c) { return __builtin_amdgcn_mfma_scale_f32_32x32x64_f8f6f4(a, b, c, 0, 0, 0, 0, 0, 0); }
; DI void attn_unit_d8(unsigned char* lds, const AttnArgs& a) {
;     ...
;     auto tile = [&](const unsigned char* Kb, const unsigned char* Kn, v8i& Pa, v8i& Pb, v8i& v0, v8i& v1, const v8i& Qa, const v8i& Qb, const v8i& w0, const v8i& w1) __attribute__((always_inline)) {
;         qk(Kb, 1, s1a, s1b);
;         v0 = rd32(Kb + voff); v1 = rd32(Kb + voff + 32 * A8_PITCH);
;         o0[0] = mfma8(w0, Qa, o0[0]); o1[0] = mfma8(w0, Qb, o1[0]); o0[1] = mfma8(w1, Qa, o0[1]); o1[1] = mfma8(w1, Qb, o1[1]);
;         expsum(s0a, l0); expsum(s0b, l1); pack4(s0a, Pa, 0); pack4(s0b, Pb, 0);
;         qk(Kn, 0, s0a, s0b);
;         expsum(s1a, l0); expsum(s1b, l1); pack4(s1a, Pa, 4); pack4(s1b, Pb, 4);
; #pragma unroll
;         for (int i = 0; i < 8; ++i) { __builtin_amdgcn_sched_group_barrier(0x008, 1, 0); __builtin_amdgcn_sched_group_barrier(0x402, 22, 0); }
;     };
;     for (int t = a.t0; t < a.t1; t += 2) {
;         const int s1 = sb + 1 >= 5 ? sb - 4 : sb + 1, s2 = sb + 2 >= 5 ? sb - 3 : sb + 2, s3 = sb + 3 >= 5 ? sb - 2 : sb + 3, s4 = sb + 4 >= 5 ? sb - 1 : sb + 4;
;         { const int ta = t + 3, tb = t + 4; gload(ta < a.t1 ? ta : a.t1 - 1, kreg0, vreg0); gload(tb < a.t1 ? tb : a.t1 - 1, kreg1, vreg1); }
;         tile(lds + sb * D8_SLOT, lds + s1 * D8_SLOT, PaX, PbX, vX0, vX1, PaY, PbY, vY0, vY1);
.LBB0_1888:
	s_add_i32 s22, s22, 2
	s_mul_i32 s8, s23, 0x2800
	s_cmp_gt_i32 s23, 3
	v_mfma_f32_32x32x64_f8f6f4 v[50:65], v[154:161], v[138:145], v[50:65]
	v_exp_f32_e32 v194, v90
	v_add_u32_e32 v90, s8, v219
	s_cselect_b32 s8, -4, 1
	s_add_i32 s51, s8, s23
	s_cmp_gt_i32 s23, 2
	s_cselect_b32 s8, -3, 2
	s_add_i32 s8, s8, s23
	s_cmp_gt_i32 s23, 1
	s_cselect_b32 s52, -2, 3
	s_add_i32 s52, s52, s23
	s_cmp_gt_i32 s23, 0
	s_cselect_b32 s53, -1, 4
	s_min_u32 s56, s22, 64
	s_add_i32 s53, s53, s23
	s_cmp_lt_u32 s22, 61
	s_mul_i32 s50, s8, 0x2800
	s_mov_b32 s23, s8
	s_cselect_b64 s[54:55], -1, 0
	s_lshl_b32 s8, s56, 6
	s_add_i32 s56, s8, 0xc0
	s_add_i32 s57, s8, 0xfffff0c0
	s_and_b64 s[54:55], s[54:55], exec
	v_lshl_add_u64 v[98:99], v[184:185], 0, s[8:9]
	s_cselect_b32 s8, s56, s57
	s_cselect_b32 s55, s19, s21
	s_cselect_b32 s54, s18, s20
	s_min_u32 s58, s22, 63
	v_exp_f32_e32 v200, v82
	v_exp_f32_e32 v201, v83
	v_exp_f32_e32 v198, v84
	v_exp_f32_e32 v199, v85
	v_exp_f32_e32 v202, v86
	v_exp_f32_e32 v203, v87
	v_exp_f32_e32 v196, v88
	v_exp_f32_e32 v197, v89
	ds_read_b128 v[82:85], v90 offset:2560
	ds_read_b128 v[86:89], v90 offset:2576
	global_load_dwordx2 v[204:205], v[98:99], off offset:192
	v_add_u32_e32 v98, s8, v182
	s_cmp_lt_u32 s22, 60
	v_ashrrev_i32_e32 v99, 31, v98
	s_cselect_b64 s[56:57], -1, 0
	s_lshl_b32 s8, s58, 6
	v_lshlrev_b64 v[98:99], 8, v[98:99]
	s_add_i32 s58, s8, 0x100
	s_add_i32 s59, s8, 0xfffff100
	v_lshl_add_u64 v[98:99], s[54:55], 0, v[98:99]
	s_and_b64 s[54:55], s[56:57], exec
	v_lshl_add_u64 v[100:101], v[184:185], 0, s[8:9]
	s_cselect_b32 s8, s58, s59
	v_lshl_add_u64 v[220:221], v[98:99], 0, v[178:179]
	v_add_u32_e32 v98, s8, v182
	v_ashrrev_i32_e32 v99, 31, v98
	s_cselect_b32 s55, s19, s21
	s_cselect_b32 s54, s18, s20
	v_lshlrev_b64 v[98:99], 8, v[98:99]
	v_lshl_add_u64 v[98:99], s[54:55], 0, v[98:99]
	global_load_dwordx2 v[206:207], v[100:101], off offset:256
	v_lshl_add_u64 v[222:223], v[98:99], 0, v[178:179]
	s_waitcnt lgkmcnt(0)
	v_mfma_f32_32x32x64_f8f6f4 v[98:113], v[82:89], v[114:121], 0
	v_exp_f32_e32 v195, v91
	v_exp_f32_e32 v224, v92
	v_exp_f32_e32 v225, v93
	v_exp_f32_e32 v226, v94
	v_exp_f32_e32 v227, v95
	v_exp_f32_e32 v228, v96
	v_exp_f32_e32 v229, v97
	ds_read_b128 v[170:173], v90 offset:5120
	ds_read_b128 v[174:177], v90 offset:5136
	ds_read_b128 v[162:165], v90 offset:7680
	ds_read_b128 v[166:169], v90 offset:7696
	v_pk_add_f32 v[90:91], v[188:189], v[200:201]
	v_pk_add_f32 v[92:93], v[186:187], v[198:199]
	v_pk_add_f32 v[90:91], v[202:203], v[90:91]
	v_pk_add_f32 v[92:93], v[196:197], v[92:93]
	v_pk_add_f32 v[90:91], v[194:195], v[90:91]
	v_pk_add_f32 v[92:93], v[224:225], v[92:93]
	v_exp_f32_e32 v66, v66
	v_exp_f32_e32 v67, v67
	v_exp_f32_e32 v68, v68
	v_exp_f32_e32 v69, v69
	v_exp_f32_e32 v70, v70
	v_exp_f32_e32 v71, v71
	v_exp_f32_e32 v72, v72
	v_pk_add_f32 v[230:231], v[228:229], v[92:93]
	v_pk_add_f32 v[232:233], v[226:227], v[90:91]
	v_mfma_f32_32x32x64_f8f6f4 v[82:97], v[82:89], v[122:129], 0
	v_exp_f32_e32 v73, v73
	v_exp_f32_e32 v74, v74
	v_exp_f32_e32 v75, v75
	v_exp_f32_e32 v76, v76
	v_exp_f32_e32 v77, v77
	v_exp_f32_e32 v78, v78
	v_exp_f32_e32 v79, v79
	v_exp_f32_e32 v80, v80
	v_exp_f32_e32 v81, v81
	v_pk_add_f32 v[188:189], v[192:193], v[66:67]
	v_pk_add_f32 v[190:191], v[190:191], v[68:69]
	s_nop 0
	v_pk_add_f32 v[188:189], v[70:71], v[188:189]
	v_pk_add_f32 v[190:191], v[72:73], v[190:191]
	s_nop 0
	v_cvt_scalef32_pk_fp8_f32 v186, v200, v201, s36
	v_pk_add_f32 v[188:189], v[74:75], v[188:189]
	v_pk_add_f32 v[190:191], v[76:77], v[190:191]
	v_cvt_scalef32_pk_fp8_f32 v187, v202, v203, s36
	v_cvt_scalef32_pk_fp8_f32 v186, v198, v199, s36 op_sel:[0,0,0,1]
	v_pk_add_f32 v[192:193], v[78:79], v[188:189]
	v_pk_add_f32 v[190:191], v[80:81], v[190:191]
	v_mfma_f32_32x32x64_f8f6f4 v[2:17], v[154:161], v[130:137], v[2:17]
	s_nop 0
	s_nop 0
	s_nop 0
	s_nop 0
	s_nop 0
	s_nop 0
	s_mulk_i32 s51, 0x2800
	v_cvt_scalef32_pk_fp8_f32 v188, v194, v195, s36
	v_cvt_scalef32_pk_fp8_f32 v189, v226, v227, s36
	v_cvt_scalef32_pk_fp8_f32 v154, v66, v67, s36
	v_cvt_scalef32_pk_fp8_f32 v155, v70, v71, s36
	v_cvt_scalef32_pk_fp8_f32 v156, v74, v75, s36
	v_cvt_scalef32_pk_fp8_f32 v157, v78, v79, s36
	v_cvt_scalef32_pk_fp8_f32 v187, v196, v197, s36 op_sel:[0,0,0,1]
	v_add_u32_e32 v234, s51, v219
	v_cvt_scalef32_pk_fp8_f32 v188, v224, v225, s36 op_sel:[0,0,0,1]
	v_cvt_scalef32_pk_fp8_f32 v189, v228, v229, s36 op_sel:[0,0,0,1]
	v_cvt_scalef32_pk_fp8_f32 v154, v68, v69, s36 op_sel:[0,0,0,1]
	v_cvt_scalef32_pk_fp8_f32 v155, v72, v73, s36 op_sel:[0,0,0,1]
	v_cvt_scalef32_pk_fp8_f32 v156, v76, v77, s36 op_sel:[0,0,0,1]
	v_cvt_scalef32_pk_fp8_f32 v157, v80, v81, s36 op_sel:[0,0,0,1]
	v_exp_f32_e32 v98, v98
	v_exp_f32_e32 v99, v99
	v_mfma_f32_32x32x64_f8f6f4 v[34:49], v[146:153], v[138:145], v[34:49]
	v_exp_f32_e32 v100, v100
	v_exp_f32_e32 v101, v101
	v_exp_f32_e32 v102, v102
	v_exp_f32_e32 v103, v103
	v_exp_f32_e32 v104, v104
	v_exp_f32_e32 v105, v105
	v_exp_f32_e32 v106, v106
	v_exp_f32_e32 v107, v107
	v_exp_f32_e32 v108, v108
	v_exp_f32_e32 v109, v109
	v_exp_f32_e32 v110, v110
	v_exp_f32_e32 v111, v111
	v_exp_f32_e32 v112, v112
	v_exp_f32_e32 v113, v113
	ds_read_b128 v[194:197], v234
	ds_read_b128 v[198:201], v234 offset:16
	v_pk_add_f32 v[66:67], v[232:233], v[98:99]
	v_pk_add_f32 v[68:69], v[230:231], v[100:101]
	v_pk_add_f32 v[66:67], v[102:103], v[66:67]
	v_pk_add_f32 v[68:69], v[104:105], v[68:69]
	v_pk_add_f32 v[66:67], v[106:107], v[66:67]
	v_pk_add_f32 v[68:69], v[108:109], v[68:69]
	v_pk_add_f32 v[140:141], v[110:111], v[66:67]
	v_pk_add_f32 v[138:139], v[112:113], v[68:69]
	v_mfma_f32_32x32x64_f8f6f4 v[18:33], v[146:153], v[130:137], v[18:33]
	v_exp_f32_e32 v82, v82
	v_exp_f32_e32 v83, v83
	v_exp_f32_e32 v84, v84
	v_exp_f32_e32 v85, v85
	v_exp_f32_e32 v86, v86
	v_exp_f32_e32 v87, v87
	v_exp_f32_e32 v88, v88
	v_exp_f32_e32 v89, v89
	v_exp_f32_e32 v90, v90
	v_exp_f32_e32 v91, v91
	v_exp_f32_e32 v92, v92
	v_exp_f32_e32 v93, v93
	v_exp_f32_e32 v94, v94
	v_exp_f32_e32 v95, v95
	v_exp_f32_e32 v96, v96
	v_exp_f32_e32 v97, v97
	v_pk_add_f32 v[66:67], v[192:193], v[82:83]
	v_pk_add_f32 v[68:69], v[190:191], v[84:85]
	v_pk_add_f32 v[66:67], v[86:87], v[66:67]
	v_pk_add_f32 v[68:69], v[88:89], v[68:69]
	v_pk_add_f32 v[130:131], v[90:91], v[66:67]
	v_pk_add_f32 v[132:133], v[92:93], v[68:69]
	s_waitcnt lgkmcnt(0)
; DI KParamsPtr kparams() { KParamsPtr p = (KParamsPtr)__builtin_amdgcn_kernarg_segment_ptr(); asm volatile("" : "+s"(p)); return p; }
; DI void attn_unit_a8(unsigned char* lds, const AttnArgs& a) {
;     ...
;     auto w_decode = [&](int j, const float*& src, unsigned char*& dst, int& ld, int& n0, int& k0, bool& gu) __attribute__((always_inline)) {
;         const int g = (j >> 2) * 512 + a.wl, e = g / 96, rr = g - e * 96; KParamsPtr kp = kparams();
;         if (rr < 64) { src = kp->w_gu + ((size_t)a.wli * NE + e) * (1024 * 2048); dst = kp->ws + WS_WGU + (size_t)a.wli * SZ_WGU + (size_t)e * 2048 * 1024; ld = 2048; n0 = (rr & 7) * 256; k0 = ((rr >> 3) * 4 + (j & 3)) * 32; gu = true; }
;         else { const int q = rr - 64; src = kp->w_dn + ((size_t)a.wli * NE + e) * (1024 * 1024); dst = kp->ws + WS_WDN + (size_t)a.wli * SZ_WDN + (size_t)e * 1024 * 1024; ld = 1024; n0 = (q & 3) * 256; k0 = ((q >> 2) * 4 + (j & 3)) * 32; gu = false; } };
;     auto w_issue = [&](int j) __attribute__((always_inline)) { const float* src; unsigned char* dst; int ld, n0, k0; bool gu; w_decode(j, src, dst, ld, n0, k0, gu);
;         const float* p = src + (size_t)(k0 + 4 * wid) * ld + n0 + wn4;
;         wq[0] = __builtin_nontemporal_load((const f32x4*)p); wq[1] = __builtin_nontemporal_load((const f32x4*)(p + ld));
;         wq[2] = __builtin_nontemporal_load((const f32x4*)(p + (size_t)2 * ld)); wq[3] = __builtin_nontemporal_load((const f32x4*)(p + (size_t)3 * ld)); };
; DI void attn_unit_d8(unsigned char* lds, const AttnArgs& a) {
;     ...
;     auto tile = [&](const unsigned char* Kb, const unsigned char* Kn, v8i& Pa, v8i& Pb, v8i& v0, v8i& v1, const v8i& Qa, const v8i& Qb, const v8i& w0, const v8i& w1) __attribute__((always_inline)) {
;         qk(Kb, 1, s1a, s1b);
;         v0 = rd32(Kb + voff); v1 = rd32(Kb + voff + 32 * A8_PITCH);
;         o0[0] = mfma8(w0, Qa, o0[0]); o1[0] = mfma8(w0, Qb, o1[0]); o0[1] = mfma8(w1, Qa, o0[1]); o1[1] = mfma8(w1, Qb, o1[1]);
;         expsum(s0a, l0); expsum(s0b, l1); pack4(s0a, Pa, 0); pack4(s0b, Pb, 0);
;         qk(Kn, 0, s0a, s0b);
;         expsum(s1a, l0); expsum(s1b, l1); pack4(s1a, Pa, 4); pack4(s1b, Pb, 4);
; #pragma unroll
;         for (int i = 0; i < 8; ++i) { __builtin_amdgcn_sched_group_barrier(0x008, 1, 0); __builtin_amdgcn_sched_group_barrier(0x402, 22, 0); }
;     };
	v_mfma_f32_32x32x64_f8f6f4 v[66:81], v[194:201], v[114:121], 0
	s_nop 0
	s_nop 0
	s_nop 0
	s_nop 0
	s_nop 0
	s_nop 0
	s_nop 0
	v_cvt_scalef32_pk_fp8_f32 v190, v98, v99, s36
	v_cvt_scalef32_pk_fp8_f32 v191, v102, v103, s36
	v_cvt_scalef32_pk_fp8_f32 v192, v106, v107, s36
	v_cvt_scalef32_pk_fp8_f32 v193, v110, v111, s36
	v_cvt_scalef32_pk_fp8_f32 v158, v82, v83, s36
	v_cvt_scalef32_pk_fp8_f32 v159, v86, v87, s36
	v_pk_add_f32 v[142:143], v[96:97], v[132:133]
	v_pk_add_f32 v[144:145], v[94:95], v[130:131]
	v_cvt_scalef32_pk_fp8_f32 v160, v90, v91, s36
	v_cvt_scalef32_pk_fp8_f32 v190, v100, v101, s36 op_sel:[0,0,0,1]
	v_cvt_scalef32_pk_fp8_f32 v191, v104, v105, s36 op_sel:[0,0,0,1]
	v_cvt_scalef32_pk_fp8_f32 v192, v108, v109, s36 op_sel:[0,0,0,1]
	v_cvt_scalef32_pk_fp8_f32 v193, v112, v113, s36 op_sel:[0,0,0,1]
	v_cvt_scalef32_pk_fp8_f32 v158, v84, v85, s36 op_sel:[0,0,0,1]
	v_cvt_scalef32_pk_fp8_f32 v159, v88, v89, s36 op_sel:[0,0,0,1]
	v_mfma_f32_32x32x64_f8f6f4 v[98:113], v[194:201], v[122:129], 0
	global_load_dwordx2 v[194:195], v[220:221], off
	global_load_dwordx2 v[196:197], v[222:223], off
	ds_read_b128 v[130:133], v234 offset:2560
	ds_read_b128 v[134:137], v234 offset:2576
	v_exp_f32_e32 v146, v66
	s_add_i32 s80, s61, 6
	v_exp_f32_e32 v147, v67
	s_lshr_b32 s73, s80, 2
	s_mulk_i32 s52, 0x2800
	s_nop 0
	s_add_i32 s8, s52, 0
	v_cvt_scalef32_pk_fp8_f32 v161, v94, v95, s36
	v_add_u32_e32 v224, s8, v183
	v_cvt_scalef32_pk_fp8_f32 v160, v92, v93, s36 op_sel:[0,0,0,1]
	v_cvt_scalef32_pk_fp8_f32 v161, v96, v97, s36 op_sel:[0,0,0,1]
	v_exp_f32_e32 v148, v68
	s_lshl_b32 s73, s73, 9
	v_exp_f32_e32 v149, v69
	s_add_i32 s73, s73, s46
	v_exp_f32_e32 v150, v70
	s_mul_i32 s75, s73, 0xaaab
	v_exp_f32_e32 v151, v71
	s_lshr_b32 s75, s75, 22
	v_exp_f32_e32 v152, v72
	s_mul_i32 s76, s75, 0x60
	v_exp_f32_e32 v153, v73
	s_sub_i32 s76, s73, s76
	v_exp_f32_e32 v198, v74
	s_lshr_b32 s77, s76, 6
	v_exp_f32_e32 v199, v75
	s_lshl_b32 s78, s77, 6
	v_exp_f32_e32 v200, v76
	s_sub_i32 s76, s76, s78
	v_exp_f32_e32 v201, v77
	s_sub_i32 s78, 3, s77
	v_exp_f32_e32 v202, v78
	s_lshr_b32 s79, s76, s78
	v_exp_f32_e32 v203, v79
	s_lshl_b32 s79, s79, 2
	v_exp_f32_e32 v220, v80
	s_and_b32 s81, s80, 3
	v_exp_f32_e32 v221, v81
	s_add_i32 s79, s79, s81
	v_pk_add_f32 v[66:67], v[140:141], v[146:147]
	s_waitcnt lgkmcnt(0)
	v_mfma_f32_32x32x64_f8f6f4 v[82:97], v[130:137], v[114:121], 0
	v_add_f32_e64 v68, v138, v148
	v_add_f32_e64 v69, v139, v149
	v_add_f32_e64 v66, v150, v66
	v_add_f32_e64 v67, v151, v67
	v_add_f32_e64 v68, v152, v68
	v_add_f32_e64 v69, v153, v69
	v_add_f32_e64 v138, v198, v66
	v_add_f32_e64 v139, v199, v67
	v_add_f32_e64 v140, v200, v68
	v_add_f32_e64 v141, v201, v69
	v_exp_f32_e32 v98, v98
	s_lshl_b32 s79, s79, 5
	v_exp_f32_e32 v99, v99
	s_lshl_b32 s81, s63, 2
	v_exp_f32_e32 v100, v100
	s_add_i32 s81, s81, s79
	v_exp_f32_e32 v101, v101
	s_sub_i32 s78, 13, s77
	v_exp_f32_e32 v102, v102
	s_lshl_b32 s81, s81, s78
	v_exp_f32_e32 v103, v103
	s_lshr_b32 s78, 7, s77
	v_exp_f32_e32 v104, v104
	s_and_b32 s78, s76, s78
	v_exp_f32_e32 v105, v105
	s_lshl_b32 s72, s78, 10
	v_exp_f32_e32 v106, v106
	s_add_i32 s81, s81, s72
	v_exp_f32_e32 v107, v107
	s_add_i32 s72, s75, 32
	v_exp_f32_e32 v108, v108
	s_sub_i32 s80, 23, s77
	v_exp_f32_e32 v109, v109
	s_lshl_b32 s72, s72, s80
	v_exp_f32_e32 v110, v110
	s_add_i32 s81, s81, s72
	v_exp_f32_e32 v111, v111
	s_cmp_eq_u32 s77, 0
	s_cselect_b64 s[84:85], s[66:67], s[68:69]
	v_exp_f32_e32 v112, v112
	s_add_u32 s84, s84, s81
	s_addc_u32 s85, s85, 0
	v_exp_f32_e32 v113, v113
	s_lshr_b32 s80, 0x2000, s77
	v_exp_f32_e32 v82, v82
	s_and_b32 s72, s78, 3
	v_mfma_f32_32x32x64_f8f6f4 v[66:81], v[130:137], v[122:129], 0
	v_add_f32_e64 v130, v144, v98
	v_add_f32_e64 v131, v145, v99
	v_add_f32_e64 v132, v142, v100
	v_add_f32_e64 v133, v143, v101
	v_add_f32_e64 v142, v102, v130
	v_add_f32_e64 v143, v103, v131
	v_add_f32_e64 v132, v104, v132
	v_add_f32_e64 v133, v105, v133
	v_add_f32_e64 v134, v220, v140
	v_add_f32_e64 v135, v221, v141
	v_add_f32_e64 v136, v202, v138
	v_add_f32_e64 v137, v203, v139
	s_nop 0
	s_nop 0
	s_nop 0
	s_nop 0
	s_nop 0
	s_nop 0
	v_pk_add_f32 v[142:143], v[106:107], v[142:143]
	v_pk_add_f32 v[132:133], v[108:109], v[132:133]
	v_cvt_scalef32_pk_fp8_f32 v138, v146, v147, s36
	v_cvt_scalef32_pk_fp8_f32 v139, v150, v151, s36
	v_cvt_scalef32_pk_fp8_f32 v140, v198, v199, s36
	v_cvt_scalef32_pk_fp8_f32 v141, v202, v203, s36
	v_cvt_scalef32_pk_fp8_f32 v130, v98, v99, s36
	v_cvt_scalef32_pk_fp8_f32 v131, v102, v103, s36
	v_pk_add_f32 v[146:147], v[112:113], v[132:133]
	v_pk_add_f32 v[150:151], v[110:111], v[142:143]
	v_mfma_f32_32x32x64_f8f6f4 v[50:65], v[170:177], v[186:193], v[50:65]
	v_exp_f32_e32 v83, v83
	s_lshl_b32 s72, s72, 19
	v_exp_f32_e32 v84, v84
	s_lshr_b32 s81, s78, 2
	v_exp_f32_e32 v85, v85
	s_lshl_b32 s81, s81, 17
	v_add_u32_e32 v102, s50, v219
	v_exp_f32_e32 v86, v86
	s_add_i32 s72, s72, s81
	v_exp_f32_e32 v87, v87
	s_lshl_b32 s81, s78, 18
	v_exp_f32_e32 v88, v88
	s_cmp_eq_u32 s77, 0
	s_cselect_b32 s72, s72, s81
; DI unsigned pk4_fp8_mul64(float a, float b, float c, float d) { v2s_t r = {0, 0}; r = __builtin_amdgcn_cvt_scalef32_pk_fp8_f32(r, a, b, 0.015625f, false); r = __builtin_amdgcn_cvt_scalef32_pk_fp8_f32(r, c, d, 0.015625f, true); return __builtin_bit_cast(unsigned, r); }
; DI f32x16 mfma8(v8i a, v8i b, f32x16 c) { return __builtin_amdgcn_mfma_scale_f32_32x32x64_f8f6f4(a, b, c, 0, 0, 0, 0, 0, 0); }
; DI void attn_unit_a8(unsigned char* lds, const AttnArgs& a) {
;     ...
;     auto w_cvt = [&]() __attribute__((always_inline)) { unsigned char* t8 = lds + AT_WT + wn4 * WPITCH + 4 * wid;
; #pragma unroll
;         for (int j = 0; j < 4; ++j) *(unsigned*)(t8 + j * WPITCH) = pk4_fp8_mul64(wq[0][j], wq[1][j], wq[2][j], wq[3][j]); };
;     const int wcol = tid >> 1, whalf = tid & 1;
;     const unsigned wper_gu = (unsigned)((wcol >> 7) * 256 + (wcol & 96) + invperm32(wcol & 31)) * 1024u + 16u * whalf;
;     const unsigned wper_dn = (unsigned)fwd_lane16(wcol) * 1024u + 16u * whalf;
;     auto w_store = [&](int j) __attribute__((always_inline)) { const float* src; unsigned char* dst; int ld, n0, k0; bool gu; w_decode(j, src, dst, ld, n0, k0, gu);
;         const int nb = n0 >> 8; const unsigned uni = (unsigned)(gu ? (nb & 3) * 512 + (nb >> 2) * 128 : nb * 256) * 1024u + (unsigned)k0;
;         const unsigned off = (gu ? wper_gu : wper_dn) + uni;
;         const unsigned* t = (const unsigned*)(lds + AT_WT + wcol * WPITCH + 16 * whalf);
;         *(u32x4*)(dst + off) = (u32x4){t[0], t[1], t[2], t[3]}; };
; DI void attn_unit_d8(unsigned char* lds, const AttnArgs& a) {
;     ...
;     auto tile = [&](const unsigned char* Kb, const unsigned char* Kn, v8i& Pa, v8i& Pb, v8i& v0, v8i& v1, const v8i& Qa, const v8i& Qb, const v8i& w0, const v8i& w1) __attribute__((always_inline)) {
;         qk(Kb, 1, s1a, s1b);
;         v0 = rd32(Kb + voff); v1 = rd32(Kb + voff + 32 * A8_PITCH);
;         o0[0] = mfma8(w0, Qa, o0[0]); o1[0] = mfma8(w0, Qb, o1[0]); o0[1] = mfma8(w1, Qa, o0[1]); o1[1] = mfma8(w1, Qb, o1[1]);
;         expsum(s0a, l0); expsum(s0b, l1); pack4(s0a, Pa, 0); pack4(s0b, Pb, 0);
;         qk(Kn, 0, s0a, s0b);
;         expsum(s1a, l0); expsum(s1b, l1); pack4(s1a, Pa, 4); pack4(s1b, Pb, 4);
; #pragma unroll
;         for (int i = 0; i < 8; ++i) { __builtin_amdgcn_sched_group_barrier(0x008, 1, 0); __builtin_amdgcn_sched_group_barrier(0x402, 22, 0); }
;     };
	v_exp_f32_e32 v89, v89
	s_mul_i32 s81, s77, 0xc000000
	v_cvt_scalef32_pk_fp8_f32 v130, v100, v101, s36 op_sel:[0,0,0,1]
	v_cvt_scalef32_pk_fp8_f32 v131, v104, v105, s36 op_sel:[0,0,0,1]
	v_exp_f32_e32 v90, v90
	s_add_i32 s81, s81, 0x9094000
	v_exp_f32_e32 v91, v91
	s_add_i32 s72, s72, s79
	v_exp_f32_e32 v92, v92
	s_sub_i32 s73, 21, s77
	v_exp_f32_e32 v93, v93
	s_lshl_b32 s73, s75, s73
	ds_read_b128 v[98:101], v102
	ds_read_b128 v[102:105], v102 offset:16
	s_nop 0
	v_cvt_scalef32_pk_fp8_f32 v138, v148, v149, s36 op_sel:[0,0,0,1]
	v_cvt_scalef32_pk_fp8_f32 v139, v152, v153, s36 op_sel:[0,0,0,1]
	v_cvt_scalef32_pk_fp8_f32 v140, v200, v201, s36 op_sel:[0,0,0,1]
	v_cvt_scalef32_pk_fp8_f32 v141, v220, v221, s36 op_sel:[0,0,0,1]
	s_nop 0
	v_exp_f32_e32 v94, v94
	s_add_i32 s72, s72, s73
	v_exp_f32_e32 v95, v95
	s_add_u32 s72, s72, s81
	v_mfma_f32_32x32x64_f8f6f4 v[2:17], v[170:177], v[154:161], v[2:17]
	v_exp_f32_e32 v148, v96
	s_or_b32 s79, s72, s77
	v_cvt_scalef32_pk_fp8_f32 v132, v106, v107, s36
	v_exp_f32_e32 v149, v97
	v_pk_add_f32 v[96:97], v[136:137], v[82:83]
	v_pk_add_f32 v[106:107], v[134:135], v[84:85]
	v_exp_f32_e32 v66, v66
	v_exp_f32_e32 v67, v67
	v_exp_f32_e32 v68, v68
	v_exp_f32_e32 v69, v69
	v_cvt_scalef32_pk_fp8_f32 v133, v110, v111, s36
	v_pk_add_f32 v[106:107], v[88:89], v[106:107]
	v_pk_add_f32 v[96:97], v[86:87], v[96:97]
	v_exp_f32_e32 v70, v70
	v_exp_f32_e32 v71, v71
	v_exp_f32_e32 v72, v72
	v_exp_f32_e32 v73, v73
	v_cvt_scalef32_pk_fp8_f32 v132, v108, v109, s36 op_sel:[0,0,0,1]
	v_cvt_scalef32_pk_fp8_f32 v133, v112, v113, s36 op_sel:[0,0,0,1]
	v_pk_add_f32 v[96:97], v[90:91], v[96:97]
	v_pk_add_f32 v[106:107], v[92:93], v[106:107]
	v_exp_f32_e32 v74, v74
	v_exp_f32_e32 v75, v75
	v_mfma_f32_32x32x64_f8f6f4 v[34:49], v[162:169], v[186:193], v[34:49]
	v_exp_f32_e32 v76, v76
	v_exp_f32_e32 v77, v77
	v_exp_f32_e32 v78, v78
	v_exp_f32_e32 v79, v79
	s_nop 0
	v_exp_f32_e32 v80, v80
	v_exp_f32_e32 v81, v81
	s_nop 0
	s_nop 0
	v_cvt_scalef32_pk_fp8_f32 v142, v82, v83, s36
	s_nop 0
	v_cvt_scalef32_pk_fp8_f32 v143, v86, v87, s36
	v_cvt_scalef32_pk_fp8_f32 v144, v90, v91, s36
	v_cvt_scalef32_pk_fp8_f32 v142, v84, v85, s36 op_sel:[0,0,0,1]
	v_pk_add_f32 v[82:83], v[150:151], v[66:67]
	v_pk_add_f32 v[84:85], v[146:147], v[68:69]
	s_mulk_i32 s53, 0x2800
	v_pk_add_f32 v[186:187], v[148:149], v[106:107]
	v_pk_add_f32 v[188:189], v[94:95], v[96:97]
	v_cvt_scalef32_pk_fp8_f32 v145, v94, v95, s36
	v_cvt_scalef32_pk_fp8_f32 v143, v88, v89, s36 op_sel:[0,0,0,1]
	v_cvt_scalef32_pk_fp8_f32 v144, v92, v93, s36 op_sel:[0,0,0,1]
	v_pk_add_f32 v[84:85], v[72:73], v[84:85]
	v_mfma_f32_32x32x64_f8f6f4 v[18:33], v[162:169], v[154:161], v[18:33]
	v_add_f32_e64 v82, v70, v82
	v_add_f32_e64 v83, v71, v83
	s_nop 0
	s_nop 0
	s_nop 0
	s_nop 0
	s_add_i32 s51, s53, 0
	v_add_f32_e64 v82, v74, v82
	v_add_f32_e64 v83, v75, v83
	v_add_f32_e64 v84, v76, v84
	v_add_f32_e64 v85, v77, v85
	v_cvt_scalef32_pk_fp8_f32 v134, v66, v67, s36
	v_cvt_scalef32_pk_fp8_f32 v135, v70, v71, s36
	v_cvt_scalef32_pk_fp8_f32 v136, v74, v75, s36
	v_cvt_scalef32_pk_fp8_f32 v137, v78, v79, s36
	v_pk_add_f32 v[190:191], v[80:81], v[84:85]
	v_pk_add_f32 v[192:193], v[78:79], v[82:83]
	v_add_u32_e32 v106, s8, v218
	v_add_u32_e32 v107, s51, v183
	v_cvt_scalef32_pk_fp8_f32 v145, v148, v149, s36 op_sel:[0,0,0,1]
	v_cvt_scalef32_pk_fp8_f32 v134, v68, v69, s36 op_sel:[0,0,0,1]
	v_cvt_scalef32_pk_fp8_f32 v135, v72, v73, s36 op_sel:[0,0,0,1]
	v_cvt_scalef32_pk_fp8_f32 v136, v76, v77, s36 op_sel:[0,0,0,1]
	v_cvt_scalef32_pk_fp8_f32 v137, v80, v81, s36 op_sel:[0,0,0,1]
	s_waitcnt lgkmcnt(0)
	v_mfma_f32_32x32x64_f8f6f4 v[82:97], v[98:105], v[114:121], 0
	ds_read_b128 v[154:157], v234 offset:5120
	ds_read_b128 v[158:161], v234 offset:5136
	ds_read_b128 v[146:149], v234 offset:7680
	ds_read_b128 v[150:153], v234 offset:7696
	s_cmpk_gt_i32 s46, 0x1ff
	s_cbranch_scc1 .Lmy_rd1_ldum
	s_add_i32 s72, s61, -1
	s_cmp_lt_u32 s72, 18
	s_cbranch_scc0 .Lmy_rd1_noc
	s_waitcnt vmcnt(4)
	v_cvt_scalef32_pk_fp8_f32 v236, v236, v240, s62
	v_cvt_scalef32_pk_fp8_f32 v237, v237, v241, s62
	v_cvt_scalef32_pk_fp8_f32 v238, v238, v242, s62
	v_cvt_scalef32_pk_fp8_f32 v239, v239, v243, s62
	v_cvt_scalef32_pk_fp8_f32 v236, v244, v248, s62 op_sel:[0,0,0,1]
	v_cvt_scalef32_pk_fp8_f32 v237, v245, v249, s62 op_sel:[0,0,0,1]
	v_cvt_scalef32_pk_fp8_f32 v238, v246, v250, s62 op_sel:[0,0,0,1]
	v_cvt_scalef32_pk_fp8_f32 v239, v247, v251, s62 op_sel:[0,0,0,1]
	ds_write_b32 v252, v236
	ds_write_b32 v252, v237 offset:36
	ds_write_b32 v252, v238 offset:72
	ds_write_b32 v252, v239 offset:108
.Lmy_rd1_noc:
	ds_read2_b32 v[244:245], v253 offset1:1
	ds_read2_b32 v[246:247], v253 offset0:2 offset1:3
	s_cmpk_gt_i32 s46, 0x1ff
	s_cbranch_scc1 .Lmy_rd1_sdum
	s_add_i32 s72, s61, -2
	s_cmp_lt_u32 s72, 18
	s_cbranch_scc0 .Lmy_rd1_sdum
	s_andn2_b32 s73, s65, 1
	s_add_u32 s82, s70, s73
	s_addc_u32 s83, s71, 0
	s_bitcmp1_b32 s65, 0
	s_cbranch_scc1 .Lmy_rd1_sdn
	s_waitcnt lgkmcnt(0)
	global_store_dwordx4 v254, v[244:247], s[82:83]
	s_branch .Lmy_rd1_sdone

; DI void attn_unit_a8(unsigned char* lds, const AttnArgs& a) {
;     ...
;         if (hk == 1) { w_cvt(); w_issue(wj + 1 < AT_NWT ? wj + 1 : AT_NWT - 1); }
;         if (hk == 2) w_store(wj);
;         { const int tn = t + 3; gload(tn < a.t1 ? tn : a.t1 - 1, kl, vl); }
.Lmy_rd1_sdone:
	s_cmpk_gt_i32 s46, 0x1ff
	s_cbranch_scc1 .Lmy_rd1_ld0
	s_cmp_lt_u32 s61, 18
	s_cbranch_scc1 .Lmy_rd1_lgo

; DI void attn_unit_a8(unsigned char* lds, const AttnArgs& a) {
;     ...
;     auto w_cvt = [&]() __attribute__((always_inline)) { unsigned char* t8 = lds + AT_WT + wn4 * WPITCH + 4 * wid;
; #pragma unroll
;         for (int j = 0; j < 4; ++j) *(unsigned*)(t8 + j * WPITCH) = pk4_fp8_mul64(wq[0][j], wq[1][j], wq[2][j], wq[3][j]); };
;     const int wcol = tid >> 1, whalf = tid & 1;
;     const unsigned wper_gu = (unsigned)((wcol >> 7) * 256 + (wcol & 96) + invperm32(wcol & 31)) * 1024u + 16u * whalf;
;     const unsigned wper_dn = (unsigned)fwd_lane16(wcol) * 1024u + 16u * whalf;
;     auto w_store = [&](int j) __attribute__((always_inline)) { const float* src; unsigned char* dst; int ld, n0, k0; bool gu; w_decode(j, src, dst, ld, n0, k0, gu);
;         const int nb = n0 >> 8; const unsigned uni = (unsigned)(gu ? (nb & 3) * 512 + (nb >> 2) * 128 : nb * 256) * 1024u + (unsigned)k0;
;         const unsigned off = (gu ? wper_gu : wper_dn) + uni;
;         const unsigned* t = (const unsigned*)(lds + AT_WT + wcol * WPITCH + 16 * whalf);
;         *(u32x4*)(dst + off) = (u32x4){t[0], t[1], t[2], t[3]}; };
;     const bool wrider = a.wl >= 0;
;     if (wrider) w_issue(0);
;     gload(a.t0, kregA, vregA); gload(a.t0 + 1 < a.t1 ? a.t0 + 1 : a.t0, kregB, vregB);
;     lstore(0, kregA, vregA); lstore(1, kregB, vregB);
;     __syncthreads();
;     asm volatile("" : "+v"(qf8));
;     if (a.t0 + 2 < a.t1) gload(a.t0 + 2, kregA, vregA);
;     f32x16 sx0, sx1, sy0, sy1;
;     sx0 = mfma8(kread(lds, 0), qf8, cinit); sx1 = mfma8(kread(lds, 1), qf8, cinit);
;     int slot = 0;
;     auto step = [&](int t, u32x2& kl, u32x2& vl, const u32x2& ks, const u32x2& vs, f32x16& c0, f32x16& c1, f32x16& n0, f32x16& n1, const int hk, const int wj) __attribute__((always_inline)) {
;         const int slot1 = slot == 2 ? 0 : slot + 1, slot2 = slot1 == 2 ? 0 : slot1 + 1;
;         if (hk == 1) { w_cvt(); w_issue(wj + 1 < AT_NWT ? wj + 1 : AT_NWT - 1); }
;         if (hk == 2) w_store(wj);
;         { const int tn = t + 3; gload(tn < a.t1 ? tn : a.t1 - 1, kl, vl); }
;         const unsigned char* Kb = lds + slot * AT_BUFB; const unsigned char* Kn = lds + slot1 * AT_BUFB;
;         const v8i k0 = kread(Kn, 0), k1 = kread(Kn, 1), v0 = vread(Kb, 0), v1 = vread(Kb, 1);
;         n0 = mfma8(k0, qf8, cinit); n1 = mfma8(k1, qf8, cinit);
;         expsum(c0); expsum(c1);
;         const v8i P = pack8(c0, c1);
.LBB0_1922:
	s_lshl_b32 s8, s18, 1
	s_waitcnt lgkmcnt(0)
	s_lshr_b32 s16, s18, 3
	s_and_b32 s8, s8, 0x600
	s_and_b32 s16, s16, 0x80
	s_or_b32 s8, s8, s16
	s_and_b64 s[14:15], s[14:15], exec
	v_pk_add_f32 v[54:55], v[164:165], v[108:109]
	s_cselect_b32 s8, s8, s18
	s_and_b32 s14, s50, 3
	v_pk_add_f32 v[54:55], v[154:155], v[54:55]
	s_add_i32 s14, s52, s14
	v_pk_add_f32 v[54:55], v[158:159], v[54:55]
	s_lshl_b32 s14, s14, 5
	s_lshl_b32 s8, s8, 10
	v_pk_add_f32 v[56:57], v[160:161], v[110:111]
	v_pk_add_f32 v[46:47], v[46:47], v[54:55]
	s_add_i32 s14, s8, s14
	s_add_i32 s51, s51, 1
	v_pk_add_f32 v[56:57], v[162:163], v[56:57]
	v_pk_add_f32 v[46:47], v[50:51], v[46:47]
	s_and_b64 s[12:13], s[12:13], exec
	v_pk_add_f32 v[56:57], v[152:153], v[56:57]
	v_pk_add_f32 v[40:41], v[40:41], v[46:47]
	s_cselect_b32 s18, 0, s51
	v_pk_add_f32 v[56:57], v[156:157], v[56:57]
	v_pk_add_f32 v[50:51], v[42:43], v[40:41]
	s_mul_i32 s8, s18, 0x4680
	v_pk_add_f32 v[44:45], v[44:45], v[56:57]
	v_add_u32_e32 v58, s8, v169
	v_pk_add_f32 v[110:111], v[34:35], v[50:51]
	v_add_u32_e32 v34, 0xd800, v175
	v_pk_add_f32 v[48:49], v[48:49], v[44:45]
	ds_read_b128 v[40:43], v58
	ds_read_b128 v[44:47], v58 offset:16
	v_add_u32_e32 v35, 0xd808, v175
	ds_read2_b32 v[54:55], v34 offset1:1
	ds_read2_b32 v[56:57], v35 offset1:1
	v_add_u32_e32 v50, v52, v170
	v_lshl_or_b32 v50, v50, 10, v172
	v_add_u32_e32 v50, s14, v50
	v_exp_f32_e32 v82, v82
	s_waitcnt lgkmcnt(0)
	global_store_dwordx4 v50, v[54:57], s[10:11]
	ds_read_b128 v[50:53], v58 offset:2560
	ds_read_b128 v[54:57], v58 offset:2576
	v_add_co_u32_e32 v58, vcc, s70, v148
	v_exp_f32_e32 v83, v83
	s_nop 0
	v_addc_co_u32_e32 v59, vcc, 0, v149, vcc
	global_load_dwordx2 v[136:137], v[58:59], off
	global_load_dwordx2 v[138:139], v[150:151], off offset:256
	v_exp_f32_e32 v86, v86
	v_exp_f32_e32 v87, v87
	v_exp_f32_e32 v90, v90
	v_exp_f32_e32 v91, v91
	v_exp_f32_e32 v94, v94
	v_exp_f32_e32 v95, v95
	v_exp_f32_e32 v164, v66
	v_exp_f32_e32 v165, v67
	v_exp_f32_e32 v178, v70
	v_exp_f32_e32 v179, v71
	v_exp_f32_e32 v74, v74
	v_exp_f32_e32 v75, v75
	v_exp_f32_e32 v78, v78
	v_exp_f32_e32 v79, v79
	ds_read_b128 v[148:151], v176 offset:5120
	ds_read_b128 v[152:155], v176 offset:5136
	ds_read_b128 v[156:159], v176 offset:7680
	ds_read_b128 v[160:163], v176 offset:7696
	v_exp_f32_e32 v84, v84
	v_exp_f32_e32 v85, v85
	v_exp_f32_e32 v88, v88
	v_exp_f32_e32 v89, v89
	v_exp_f32_e32 v92, v92
	v_exp_f32_e32 v93, v93
	v_exp_f32_e32 v96, v96
	v_exp_f32_e32 v97, v97
	v_exp_f32_e32 v176, v68
	v_exp_f32_e32 v177, v69
	v_exp_f32_e32 v180, v72
	v_exp_f32_e32 v181, v73
	v_exp_f32_e32 v76, v76
	v_exp_f32_e32 v77, v77
	v_exp_f32_e32 v80, v80
	v_exp_f32_e32 v81, v81
	s_nop 0
	s_nop 0
	s_nop 0
	s_nop 0
	s_nop 0
	s_nop 0
	s_nop 0
	s_nop 0
	v_cvt_scalef32_pk_fp8_f32 v66, v82, v83, s69
	v_cvt_scalef32_pk_fp8_f32 v70, v164, v165, s69
	v_cvt_scalef32_pk_fp8_f32 v67, v86, v87, s69
	v_cvt_scalef32_pk_fp8_f32 v71, v178, v179, s69
	v_cvt_scalef32_pk_fp8_f32 v68, v90, v91, s69
	v_cvt_scalef32_pk_fp8_f32 v72, v74, v75, s69
	v_cvt_scalef32_pk_fp8_f32 v69, v94, v95, s69
	v_cvt_scalef32_pk_fp8_f32 v73, v78, v79, s69
	v_pk_add_f32 v[36:37], v[36:37], v[48:49]
	v_cvt_scalef32_pk_fp8_f32 v66, v84, v85, s69 op_sel:[0,0,0,1]
	v_cvt_scalef32_pk_fp8_f32 v70, v176, v177, s69 op_sel:[0,0,0,1]
	v_cvt_scalef32_pk_fp8_f32 v67, v88, v89, s69 op_sel:[0,0,0,1]
	v_cvt_scalef32_pk_fp8_f32 v71, v180, v181, s69 op_sel:[0,0,0,1]
	v_cvt_scalef32_pk_fp8_f32 v68, v92, v93, s69 op_sel:[0,0,0,1]
	v_cvt_scalef32_pk_fp8_f32 v72, v76, v77, s69 op_sel:[0,0,0,1]
	v_cvt_scalef32_pk_fp8_f32 v69, v96, v97, s69 op_sel:[0,0,0,1]
	v_cvt_scalef32_pk_fp8_f32 v73, v80, v81, s69 op_sel:[0,0,0,1]
	v_pk_add_f32 v[108:109], v[38:39], v[36:37]
	v_mfma_f32_32x32x64_f8f6f4 v[34:49], v[40:47], v[98:105], 0
	v_add_f32_e64 v110, v110, v82
	v_add_f32_e64 v111, v111, v83
	v_add_f32_e64 v82, v108, v84
	v_add_f32_e64 v83, v109, v85
	v_add_f32_e64 v84, v86, v110
	v_add_f32_e64 v85, v87, v111
	v_add_f32_e64 v82, v88, v82
	v_add_f32_e64 v83, v89, v83
	s_addk_i32 s8, 0x4680
	v_add_f32_e64 v84, v90, v84
	v_add_f32_e64 v85, v91, v85
	v_add_f32_e64 v82, v92, v82
	v_add_f32_e64 v83, v93, v83
	s_cmp_lg_u32 s18, 2
	v_pk_add_f32 v[82:83], v[96:97], v[82:83]
	v_pk_add_f32 v[84:85], v[94:95], v[84:85]
	s_cselect_b32 s8, s8, 0
	v_pk_add_f32 v[84:85], v[164:165], v[84:85]
	v_pk_add_f32 v[82:83], v[176:177], v[82:83]
	s_add_i32 s8, s8, 0
	v_pk_add_f32 v[82:83], v[180:181], v[82:83]
	s_waitcnt lgkmcnt(4)
	v_mfma_f32_32x32x64_f8f6f4 v[50:65], v[50:57], v[98:105], 0
	v_add_f32_e64 v84, v178, v84
	v_add_f32_e64 v85, v179, v85
	v_add_f32_e64 v76, v76, v82
	v_add_f32_e64 v77, v77, v83
	v_add_f32_e64 v74, v74, v84
	v_add_f32_e64 v75, v75, v85
	s_add_i32 s50, s50, 1
	s_addk_i32 s23, 0x80
	v_add_f32_e64 v110, v80, v76
	v_add_f32_e64 v111, v81, v77
	v_add_f32_e64 v108, v78, v74
	v_add_f32_e64 v109, v79, v75
	v_lshl_add_u64 v[140:141], v[140:141], 0, s[36:37]
	s_cmp_lg_u32 s50, 6
	v_lshl_add_u64 v[142:143], v[142:143], 0, s[38:39]
	s_waitcnt lgkmcnt(2)
	v_mfma_f32_32x32x64_f8f6f4 v[18:33], v[148:155], v[66:73], v[18:33]
	s_waitcnt lgkmcnt(0)
	v_mfma_f32_32x32x64_f8f6f4 v[2:17], v[156:163], v[66:73], v[2:17]
	v_add_u32_e32 v66, s8, v131
	s_waitcnt vmcnt(4)
	ds_write_b64 v66, v[144:145]
	v_add_u32_e32 v66, s8, v168
	v_add_u32_e32 v66, 0x1400, v66
	s_waitcnt vmcnt(3)
	ds_write2_b32 v66, v146, v147 offset1:8
	s_waitcnt lgkmcnt(0)
	s_barrier
	s_cbranch_scc0 .LBB0_1931
.LBB0_1923:
	s_min_u32 s19, s50, 4
	s_add_i32 s19, s19, 1
	s_lshl_b32 s8, s19, 7
	s_and_b32 s8, s8, 0x1e00
	s_nop 0
	s_nop 0
	s_add_i32 s10, s8, s76
	v_cvt_scalef32_pk_fp8_f32 v66, v116, v112, s66
	v_cvt_scalef32_pk_fp8_f32 v67, v117, v113, s66
	s_mul_hi_u32 s8, s10, 0xaaaaaaab
	v_cvt_scalef32_pk_fp8_f32 v66, v120, v124, s66 op_sel:[0,0,0,1]
	v_cvt_scalef32_pk_fp8_f32 v67, v121, v125, s66 op_sel:[0,0,0,1]
	v_add_u32_e32 v68, 0xd800, v174
	s_lshr_b32 s8, s8, 6
	ds_write2_b32 v68, v66, v67 offset1:9
	s_nop 0
	s_nop 0
	s_mul_i32 s52, s8, 0xffffffa0
	v_cvt_scalef32_pk_fp8_f32 v66, v118, v114, s66
	v_cvt_scalef32_pk_fp8_f32 v67, v119, v115, s66
	s_add_i32 s52, s52, s10
	v_cvt_scalef32_pk_fp8_f32 v66, v122, v126, s66 op_sel:[0,0,0,1]
	v_cvt_scalef32_pk_fp8_f32 v67, v123, v127, s66 op_sel:[0,0,0,1]
	s_mov_b64 s[14:15], s[0:1]
	s_cmp_gt_i32 s52, 63
	s_mov_b64 s[16:17], -1
	ds_write2_b32 v68, v66, v67 offset0:18 offset1:27
	s_cbranch_scc0 .LBB0_1925
	s_load_dwordx2 s[10:11], s[14:15], 0xc0
	s_lshl_b64 s[12:13], s[8:9], 22
	s_mov_b64 s[16:17], 0
	s_waitcnt lgkmcnt(0)
	s_add_u32 s10, s10, s12
	s_addc_u32 s11, s11, s13
	s_add_u32 s10, s10, 0x8000000
	s_addc_u32 s11, s11, 0
	s_and_b32 s12, s52, 0x7ffffffc
	s_sub_i32 s51, s12, 64
